# counted lgkmcnt waits for the P*V transpose-read groups in mixer-B lead and mixer-A loops (each MFMA waits only for its own operand reads)
# speedup vs baseline: 1.0189x; 1.0044x over previous
; #define LAS __attribute__((address_space(3)))
; __device__ __forceinline__ void finishSM(f32x16& p0, f32x16& p1, float alpha, float& l_reg, bf16x8& pa0, bf16x8& pa1, bf16x8& pa2, bf16x8& pa3) {
; #pragma unroll
;     for (int r = 0; r < 16; ++r) p1[r] = __builtin_amdgcn_exp2f(p1[r]);
;     float ps = 0;
; #pragma unroll
;     for (int r = 0; r < 16; ++r) ps += p0[r];
; #pragma unroll
;     for (int r = 0; r < 16; ++r) ps += p1[r];
;     { auto rr = __builtin_amdgcn_permlane32_swap(__float_as_uint(ps), __float_as_uint(ps), false, false);
;       ps = __uint_as_float(rr[0]) + __uint_as_float(rr[1]); }
;     l_reg = l_reg * alpha + ps;
;     ...
;     PK4(p0, 0, pa0); PK4(p0, 8, pa1); PK4(p1, 0, pa2); PK4(p1, 8, pa3);
;     ...
; }
; template <int KB>
; __device__ __forceinline__ void qkt(f32x16& p0, f32x16& p1, const LAS char* K_lds, int r32, int hi, const bf16x8* qr) {
;     p0 = f32x16{}; p1 = f32x16{};
;     const LAS char* kb[4];
; #pragma unroll
;     for (int dd = 0; dd < 4; ++dd) kb[dd] = K_lds + KB * SHM_K + KSWZ(r32, (dd * 16 + hi * 8) * 2);
; #pragma unroll
;     for (int d0 = 0; d0 < 8; ++d0) { const LAS char* a = kb[d0 & 3] + (d0 >> 2) * 128;
;         bf16x8 b0 = *(const LAS bf16x8*)(a);
;         bf16x8 b1 = *(const LAS bf16x8*)(a + 32 * 256);
;         p0 = __builtin_amdgcn_mfma_f32_32x32x16_bf16(b0, qr[d0], p0, 0, 0, 0);
;         p1 = __builtin_amdgcn_mfma_f32_32x32x16_bf16(b1, qr[d0], p1, 0, 0, 0); }
; }
; template <int VB>
; __device__ __forceinline__ void pv_tile(f32x16* o, int vb0, bf16x8 pa0, bf16x8 pa1, bf16x8 pa2, bf16x8 pa3) {
;     ...
;     PV_D0(0); PV_D0(1); PV_D0(2); PV_D0(3);
.LBB0_1294:
	v_add_u32_e32 v0, v172, v161
	ds_read_b128 v[66:69], v0
	ds_read_b128 v[70:73], v0 offset:8192
	v_add_u32_e32 v146, v172, v163
	ds_read_b128 v[190:193], v146
	ds_read_b128 v[198:201], v146 offset:8192
	v_add_u32_e32 v175, v172, v165
	s_waitcnt lgkmcnt(3)
	v_mfma_f32_32x32x16_bf16 v[82:97], v[66:69], v[98:101], 0
	v_add_u32_e32 v176, v172, v167
	v_exp_f32_e32 v142, v142
	v_exp_f32_e32 v143, v143
	v_exp_f32_e32 v140, v140
	v_exp_f32_e32 v141, v141
	v_exp_f32_e32 v138, v138
	v_exp_f32_e32 v139, v139
	s_waitcnt lgkmcnt(2)
	v_mfma_f32_32x32x16_bf16 v[66:81], v[70:73], v[98:101], 0
	v_exp_f32_e32 v136, v136
	v_exp_f32_e32 v137, v137
	v_exp_f32_e32 v134, v134
	v_exp_f32_e32 v135, v135
	v_exp_f32_e32 v132, v132
	v_exp_f32_e32 v133, v133
	v_exp_f32_e32 v130, v130
	s_waitcnt lgkmcnt(1)
	v_mfma_f32_32x32x16_bf16 v[82:97], v[190:193], v[102:105], v[82:97]
	v_exp_f32_e32 v131, v131
	v_cvt_pk_bf16_f32 v181, v142, v143
	v_cvt_pk_bf16_f32 v182, v140, v141
	s_waitcnt lgkmcnt(0)
	v_mfma_f32_32x32x16_bf16 v[66:81], v[198:201], v[102:105], v[66:81]
	ds_read_b128 v[190:193], v175
	ds_read_b128 v[198:201], v175 offset:8192
	s_waitcnt lgkmcnt(1)
	v_mfma_f32_32x32x16_bf16 v[82:97], v[190:193], v[106:109], v[82:97]
	s_waitcnt lgkmcnt(0)
	v_mfma_f32_32x32x16_bf16 v[66:81], v[198:201], v[106:109], v[66:81]
	ds_read_b128 v[190:193], v176
	ds_read_b128 v[198:201], v176 offset:8192
	s_waitcnt lgkmcnt(1)
	v_mfma_f32_32x32x16_bf16 v[82:97], v[190:193], v[110:113], v[82:97]
	s_waitcnt lgkmcnt(0)
	v_mfma_f32_32x32x16_bf16 v[66:81], v[198:201], v[110:113], v[66:81]
	ds_read_b128 v[190:193], v0 offset:128
	ds_read_b128 v[198:201], v0 offset:8320
	v_exp_f32_e32 v0, v144
	v_exp_f32_e32 v144, v145
	v_add_f32_e32 v145, 0, v147
	v_add_f32_e32 v145, v148, v145
	v_add_f32_e32 v145, v149, v145
	v_add_f32_e32 v145, v185, v145
	s_waitcnt lgkmcnt(1)
	v_mfma_f32_32x32x16_bf16 v[82:97], v[190:193], v[114:117], v[82:97]
	v_add_f32_e32 v145, v186, v145
	v_add_f32_e32 v145, v188, v145
	v_add_f32_e32 v145, v184, v145
	v_add_f32_e32 v145, v187, v145
	v_add_f32_e32 v145, v150, v145
	v_add_f32_e32 v145, v151, v145
	v_add_f32_e32 v145, v153, v145
	s_waitcnt lgkmcnt(0)
	v_mfma_f32_32x32x16_bf16 v[66:81], v[198:201], v[114:117], v[66:81]
	ds_read_b128 v[190:193], v146 offset:128
	ds_read_b128 v[198:201], v146 offset:8320
	v_add_f32_e32 v145, v155, v145
	v_add_f32_e32 v145, v152, v145
	v_add_f32_e32 v145, v156, v145
	v_add_f32_e32 v145, v157, v145
	v_add_f32_e32 v145, v183, v145
	v_add_f32_e32 v145, v0, v145
	s_waitcnt lgkmcnt(1)
	v_mfma_f32_32x32x16_bf16 v[82:97], v[190:193], v[118:121], v[82:97]
	v_add_f32_e32 v145, v144, v145
	v_add_f32_e32 v145, v142, v145
	v_add_f32_e32 v145, v143, v145
	v_add_f32_e32 v145, v140, v145
	v_add_f32_e32 v145, v141, v145
	v_add_f32_e32 v145, v138, v145
	v_add_f32_e32 v145, v139, v145
	s_waitcnt lgkmcnt(0)
	v_mfma_f32_32x32x16_bf16 v[66:81], v[198:201], v[118:121], v[66:81]
	ds_read_b128 v[190:193], v175 offset:128
	ds_read_b128 v[198:201], v175 offset:8320
	v_add_f32_e32 v145, v136, v145
	v_add_f32_e32 v145, v137, v145
	v_add_f32_e32 v145, v134, v145
	v_add_f32_e32 v145, v135, v145
	v_add_f32_e32 v145, v132, v145
	v_add_f32_e32 v145, v133, v145
	s_waitcnt lgkmcnt(1)
	v_mfma_f32_32x32x16_bf16 v[82:97], v[190:193], v[122:125], v[82:97]
	v_add_f32_e32 v145, v130, v145
	v_add_f32_e32 v175, v131, v145
	v_cvt_pk_bf16_f32 v146, v147, v148
	v_cvt_pk_bf16_f32 v147, v149, v185
	v_cvt_pk_bf16_f32 v148, v186, v188
	v_cvt_pk_bf16_f32 v149, v184, v187
	v_cvt_pk_bf16_f32 v150, v150, v151
	s_waitcnt lgkmcnt(0)
	v_mfma_f32_32x32x16_bf16 v[66:81], v[198:201], v[122:125], v[66:81]
	ds_read_b128 v[190:193], v176 offset:128
	ds_read_b128 v[198:201], v176 offset:8320
	v_mov_b32_e32 v176, v175
	s_nop 1
	v_permlane32_swap_b32_e32 v175, v176
	v_cvt_pk_bf16_f32 v151, v153, v155
	v_cvt_pk_bf16_f32 v152, v152, v156
	v_cvt_pk_bf16_f32 v153, v157, v183
	s_waitcnt lgkmcnt(1)
	v_mfma_f32_32x32x16_bf16 v[82:97], v[190:193], v[126:129], v[82:97]
	v_cvt_pk_bf16_f32 v180, v0, v144
	v_cvt_pk_bf16_f32 v183, v138, v139
	v_cvt_pk_bf16_f32 v184, v136, v137
	v_cvt_pk_bf16_f32 v185, v134, v135
	v_cvt_pk_bf16_f32 v186, v132, v133
	v_cvt_pk_bf16_f32 v187, v130, v131
	v_permlane32_swap_b32_e32 v146, v148
	s_waitcnt lgkmcnt(0)
	v_mfma_f32_32x32x16_bf16 v[66:81], v[198:201], v[126:129], v[66:81]
	v_permlane32_swap_b32_e32 v147, v149
	v_permlane32_swap_b32_e32 v150, v152
	v_permlane32_swap_b32_e32 v151, v153
	v_permlane32_swap_b32_e32 v180, v182
	v_permlane32_swap_b32_e32 v181, v183
	v_permlane32_swap_b32_e32 v184, v186
	v_permlane32_swap_b32_e32 v185, v187
	s_mov_b32 s4, 0xffff0000
	v_add_co_u32_e32 v130, vcc, s4, v158
	s_movk_i32 s4, 0x8000
	s_nop 0
	v_addc_co_u32_e32 v131, vcc, -1, v159, vcc
	v_add_co_u32_e32 v134, vcc, s4, v158
	s_mov_b32 s4, 0x8000
	s_nop 0
	v_addc_co_u32_e32 v135, vcc, -1, v159, vcc
	v_add_co_u32_e32 v142, vcc, s4, v158
	global_load_dwordx4 v[130:133], v[130:131], off
	s_nop 0
	global_load_dwordx4 v[134:137], v[134:135], off
	v_addc_co_u32_e32 v143, vcc, 0, v159, vcc
	global_load_dwordx4 v[138:141], v[158:159], off
	s_nop 0
	global_load_dwordx4 v[142:145], v[142:143], off
	v_add_u32_e32 v0, s89, v223
	ds_write_b128 v0, v[146:149]
	ds_write_b128 v0, v[150:153] offset:16
	ds_write_b128 v0, v[180:183] offset:32
	ds_write_b128 v0, v[184:187] offset:48
	ds_read_b64_tr_b16 v[188:189], v169 offset:0
	ds_read_b64_tr_b16 v[190:191], v169 offset:0x800
	ds_read_b64_tr_b16 v[192:193], v169 offset:0x1000
	ds_read_b64_tr_b16 v[194:195], v169 offset:0x1800
	ds_read_b64_tr_b16 v[198:199], v169 offset:0x2000
	ds_read_b64_tr_b16 v[200:201], v169 offset:0x2800
	ds_read_b64_tr_b16 v[202:203], v169 offset:0x3000
	ds_read_b64_tr_b16 v[204:205], v169 offset:0x3800
	s_nop 0
	s_nop 0
	s_waitcnt lgkmcnt(6)
; __device__ __forceinline__ void mask_tile(f32x16& p0, f32x16& p1, int dq) {
;     const float NEG = -__builtin_inff();
; #pragma unroll
;     for (int r = 0; r < 16; ++r) { const int c = (r & 3) + 8 * (r >> 2); if (dq - c < 0) p0[r] = NEG; if (dq - c - 32 < 0) p1[r] = NEG; }
; }
; template <int VB>
; __device__ __forceinline__ void pv_tile(f32x16* o, int vb0, bf16x8 pa0, bf16x8 pa1, bf16x8 pa2, bf16x8 pa3) {
;     ...
;     PV_D0(0); PV_D0(1); PV_D0(2); PV_D0(3);
	v_mfma_f32_32x32x16_bf16 v[50:65], v[146:149], v[188:191], v[50:65]
	ds_read_b64_tr_b16 v[188:189], v169 offset:0x200
	ds_read_b64_tr_b16 v[190:191], v169 offset:0xa00
	s_waitcnt lgkmcnt(6)
	v_mfma_f32_32x32x16_bf16 v[50:65], v[150:153], v[192:195], v[50:65]
	ds_read_b64_tr_b16 v[192:193], v169 offset:0x1200
	ds_read_b64_tr_b16 v[194:195], v169 offset:0x1a00
	s_waitcnt lgkmcnt(6)
	v_mfma_f32_32x32x16_bf16 v[50:65], v[180:183], v[198:201], v[50:65]
	ds_read_b64_tr_b16 v[198:199], v169 offset:0x2200
	ds_read_b64_tr_b16 v[200:201], v169 offset:0x2a00
	s_waitcnt lgkmcnt(6)
	v_mfma_f32_32x32x16_bf16 v[50:65], v[184:187], v[202:205], v[50:65]
	ds_read_b64_tr_b16 v[202:203], v169 offset:0x3200
	ds_read_b64_tr_b16 v[204:205], v169 offset:0x3a00
	s_nop 0
	s_waitcnt lgkmcnt(6)
	v_mfma_f32_32x32x16_bf16 v[34:49], v[146:149], v[188:191], v[34:49]
	ds_read_b64_tr_b16 v[188:189], v169 offset:0x400
	ds_read_b64_tr_b16 v[190:191], v169 offset:0xc00
	s_waitcnt lgkmcnt(6)
	v_mfma_f32_32x32x16_bf16 v[34:49], v[150:153], v[192:195], v[34:49]
	ds_read_b64_tr_b16 v[192:193], v169 offset:0x1400
	ds_read_b64_tr_b16 v[194:195], v169 offset:0x1c00
	s_waitcnt lgkmcnt(6)
	v_mfma_f32_32x32x16_bf16 v[34:49], v[180:183], v[198:201], v[34:49]
	ds_read_b64_tr_b16 v[198:199], v169 offset:0x2400
	ds_read_b64_tr_b16 v[200:201], v169 offset:0x2c00
	s_waitcnt lgkmcnt(6)
	v_mfma_f32_32x32x16_bf16 v[34:49], v[184:187], v[202:205], v[34:49]
	ds_read_b64_tr_b16 v[202:203], v169 offset:0x3400
	ds_read_b64_tr_b16 v[204:205], v169 offset:0x3c00
	s_nop 0
	s_waitcnt lgkmcnt(6)
	v_mfma_f32_32x32x16_bf16 v[18:33], v[146:149], v[188:191], v[18:33]
	ds_read_b64_tr_b16 v[188:189], v169 offset:0x600
	ds_read_b64_tr_b16 v[190:191], v169 offset:0xe00
	s_waitcnt lgkmcnt(6)
	v_mfma_f32_32x32x16_bf16 v[18:33], v[150:153], v[192:195], v[18:33]
	ds_read_b64_tr_b16 v[192:193], v169 offset:0x1600
	ds_read_b64_tr_b16 v[194:195], v169 offset:0x1e00
	s_waitcnt lgkmcnt(6)
	v_mfma_f32_32x32x16_bf16 v[18:33], v[180:183], v[198:201], v[18:33]
	ds_read_b64_tr_b16 v[198:199], v169 offset:0x2600
	ds_read_b64_tr_b16 v[200:201], v169 offset:0x2e00
	s_waitcnt lgkmcnt(6)
	v_mfma_f32_32x32x16_bf16 v[18:33], v[184:187], v[202:205], v[18:33]
	ds_read_b64_tr_b16 v[202:203], v169 offset:0x3600
	ds_read_b64_tr_b16 v[204:205], v169 offset:0x3e00
	s_nop 0
	s_waitcnt lgkmcnt(6)
	v_mfma_f32_32x32x16_bf16 v[2:17], v[146:149], v[188:191], v[2:17]
	s_cmp_le_u32 s79, s68
	s_waitcnt lgkmcnt(4)
	v_mfma_f32_32x32x16_bf16 v[2:17], v[150:153], v[192:195], v[2:17]
	s_waitcnt lgkmcnt(2)
	v_mfma_f32_32x32x16_bf16 v[2:17], v[180:183], v[198:201], v[2:17]
	s_waitcnt lgkmcnt(0)
	v_mfma_f32_32x32x16_bf16 v[2:17], v[184:187], v[202:205], v[2:17]
	s_cbranch_scc1 .LBB0_1296
	v_cmp_gt_i32_e64 s[62:63], 26, v174
	v_cmp_gt_i32_e64 s[64:65], 27, v174
	v_cmp_gt_i32_e64 s[60:61], 25, v174
	s_and_b64 s[62:63], s[64:65], s[62:63]
	v_cmp_gt_i32_e64 s[58:59], 24, v174
	s_and_b64 s[60:61], s[62:63], s[60:61]
	v_cmp_gt_i32_e64 s[56:57], 19, v174
	s_and_b64 s[58:59], s[60:61], s[58:59]
	v_cmp_gt_i32_e64 s[54:55], 18, v174
	s_and_b64 s[56:57], s[58:59], s[56:57]
	v_cmp_gt_i32_e64 s[52:53], 17, v174
	s_and_b64 s[54:55], s[56:57], s[54:55]
	v_cmp_gt_i32_e64 s[50:51], 16, v174
	s_and_b64 s[52:53], s[54:55], s[52:53]
	v_cmp_gt_i32_e64 s[48:49], 11, v174
	s_and_b64 s[50:51], s[52:53], s[50:51]
	v_cmp_gt_i32_e64 s[46:47], 10, v174
	s_and_b64 s[48:49], s[50:51], s[48:49]
	v_cmp_gt_i32_e64 s[44:45], 9, v174
	s_and_b64 s[46:47], s[48:49], s[46:47]
	v_cmp_gt_i32_e64 s[42:43], 8, v174
	s_and_b64 s[44:45], s[46:47], s[44:45]
	v_cmp_gt_i32_e64 s[40:41], 3, v174
	s_and_b64 s[42:43], s[44:45], s[42:43]
	v_cmp_gt_i32_e64 s[38:39], 2, v174
	s_and_b64 s[40:41], s[42:43], s[40:41]
	v_cmp_gt_i32_e64 s[36:37], 1, v174
	s_and_b64 s[38:39], s[40:41], s[38:39]
	v_cmp_gt_i32_e64 s[34:35], 0, v174
	s_and_b64 s[36:37], s[38:39], s[36:37]
	s_and_b64 s[34:35], s[36:37], s[34:35]
	v_cmp_gt_i32_e64 s[30:31], 58, v174
	v_cndmask_b32_e64 v82, v82, v197, s[34:35]
	v_cmp_gt_i32_e64 s[34:35], 59, v174
	v_cmp_gt_i32_e64 s[28:29], 57, v174
	s_and_b64 s[30:31], s[34:35], s[30:31]
	v_cmp_gt_i32_e64 s[26:27], 56, v174
	s_and_b64 s[28:29], s[30:31], s[28:29]
	v_cmp_gt_i32_e64 s[24:25], 51, v174
	s_and_b64 s[26:27], s[28:29], s[26:27]
	v_cmp_gt_i32_e64 s[22:23], 50, v174
	s_and_b64 s[24:25], s[26:27], s[24:25]
	v_cmp_gt_i32_e64 s[20:21], 49, v174
	s_and_b64 s[22:23], s[24:25], s[22:23]
	v_cmp_gt_i32_e64 s[18:19], 48, v174
	s_and_b64 s[20:21], s[22:23], s[20:21]
	v_cmp_gt_i32_e64 s[16:17], 43, v174
	s_and_b64 s[18:19], s[20:21], s[18:19]
	v_cmp_gt_i32_e64 s[14:15], 42, v174
	s_and_b64 s[16:17], s[18:19], s[16:17]
	v_cmp_gt_i32_e64 s[12:13], 41, v174
	s_and_b64 s[14:15], s[16:17], s[14:15]
	v_cmp_gt_i32_e64 s[10:11], 40, v174
	s_and_b64 s[12:13], s[14:15], s[12:13]
	v_cmp_gt_i32_e64 s[8:9], 35, v174
	s_and_b64 s[10:11], s[12:13], s[10:11]
	v_cmp_gt_i32_e64 s[6:7], 34, v174
	s_and_b64 s[8:9], s[10:11], s[8:9]
	v_cmp_gt_i32_e64 s[4:5], 33, v174
	s_and_b64 s[6:7], s[8:9], s[6:7]
	v_cmp_gt_i32_e32 vcc, 32, v174
	s_and_b64 s[4:5], s[6:7], s[4:5]
	s_and_b64 vcc, s[4:5], vcc
	v_cndmask_b32_e64 v97, v97, v197, s[64:65]
	v_cndmask_b32_e64 v96, v96, v197, s[62:63]
	v_cndmask_b32_e64 v95, v95, v197, s[60:61]
	v_cndmask_b32_e64 v94, v94, v197, s[58:59]
	v_cndmask_b32_e64 v93, v93, v197, s[56:57]
	v_cndmask_b32_e64 v92, v92, v197, s[54:55]
	v_cndmask_b32_e64 v91, v91, v197, s[52:53]
	v_cndmask_b32_e64 v90, v90, v197, s[50:51]
	v_cndmask_b32_e64 v89, v89, v197, s[48:49]
	v_cndmask_b32_e64 v88, v88, v197, s[46:47]
	v_cndmask_b32_e64 v87, v87, v197, s[44:45]
	v_cndmask_b32_e64 v86, v86, v197, s[42:43]
	v_cndmask_b32_e64 v85, v85, v197, s[40:41]
	v_cndmask_b32_e64 v84, v84, v197, s[38:39]
	v_cndmask_b32_e64 v83, v83, v197, s[36:37]
	v_cndmask_b32_e64 v81, v81, v197, s[34:35]
	v_cndmask_b32_e64 v80, v80, v197, s[30:31]
	v_cndmask_b32_e64 v79, v79, v197, s[28:29]
	v_cndmask_b32_e64 v78, v78, v197, s[26:27]
	v_cndmask_b32_e64 v77, v77, v197, s[24:25]
	v_cndmask_b32_e64 v76, v76, v197, s[22:23]
	v_cndmask_b32_e64 v75, v75, v197, s[20:21]
	v_cndmask_b32_e64 v74, v74, v197, s[18:19]
	v_cndmask_b32_e64 v73, v73, v197, s[16:17]
	v_cndmask_b32_e64 v72, v72, v197, s[14:15]
	v_cndmask_b32_e64 v71, v71, v197, s[12:13]
	v_cndmask_b32_e64 v70, v70, v197, s[10:11]
	v_cndmask_b32_e64 v69, v69, v197, s[8:9]
	v_cndmask_b32_e64 v68, v68, v197, s[6:7]
	v_cndmask_b32_e64 v67, v67, v197, s[4:5]
	v_cndmask_b32_e32 v66, v66, v197, vcc

; #define LAS __attribute__((address_space(3)))
; __device__ __forceinline__ void partialSM(f32x16& p0, f32x16& p1, float& m_reg, float& mn, float& alpha) {
;     float pmax = p0[0];
; #pragma unroll
;     for (int r = 1; r < 16; ++r) pmax = fmaxf(pmax, p0[r]);
; #pragma unroll
;     for (int r = 0; r < 16; ++r) pmax = fmaxf(pmax, p1[r]);
;     { auto rr = __builtin_amdgcn_permlane32_swap(__float_as_uint(pmax), __float_as_uint(pmax), false, false);
;       pmax = fmaxf(__uint_as_float(rr[0]), __uint_as_float(rr[1])); }
;     constexpr float C2 = 1.4426950408889634f * SCALE;
;     if (__builtin_expect(__all((pmax - m_reg) * SCALE <= THR), 1)) { mn = m_reg; alpha = 1.f; }
;     else { mn = fmaxf(m_reg, pmax); alpha = __builtin_amdgcn_exp2f((m_reg - mn) * C2); m_reg = mn; }
;     const float mnL = -mn * C2;
; #pragma unroll
;     for (int r = 0; r < 16; ++r) p0[r] = fmaf(p0[r], C2, mnL);
; #pragma unroll
;     for (int r = 0; r < 16; ++r) p1[r] = fmaf(p1[r], C2, mnL);
; #pragma unroll
;     for (int r = 0; r < 16; ++r) p0[r] = __builtin_amdgcn_exp2f(p0[r]);
; }
; template <int KB>
; __device__ __forceinline__ void qkt(f32x16& p0, f32x16& p1, const LAS char* K_lds, int r32, int hi, const bf16x8* qr) {
;     p0 = f32x16{}; p1 = f32x16{};
;     const LAS char* kb[4];
; #pragma unroll
;     for (int dd = 0; dd < 4; ++dd) kb[dd] = K_lds + KB * SHM_K + KSWZ(r32, (dd * 16 + hi * 8) * 2);
; #pragma unroll
;     for (int d0 = 0; d0 < 8; ++d0) { const LAS char* a = kb[d0 & 3] + (d0 >> 2) * 128;
;         bf16x8 b0 = *(const LAS bf16x8*)(a);
;         bf16x8 b1 = *(const LAS bf16x8*)(a + 32 * 256);
;         p0 = __builtin_amdgcn_mfma_f32_32x32x16_bf16(b0, qr[d0], p0, 0, 0, 0);
;         p1 = __builtin_amdgcn_mfma_f32_32x32x16_bf16(b1, qr[d0], p1, 0, 0, 0); }
; }
.LBB0_1302:
	v_cndmask_b32_e64 v180, v146, v154, s[4:5]
	s_waitcnt lgkmcnt(0)
	v_mul_f32_e32 v138, 0xbe0293ee, v180
	v_fmamk_f32 v82, v82, 0x3e0293ee, v138
	v_fmamk_f32 v83, v83, 0x3e0293ee, v138
	v_fmamk_f32 v84, v84, 0x3e0293ee, v138
	v_fmamk_f32 v85, v85, 0x3e0293ee, v138
	v_fmamk_f32 v86, v86, 0x3e0293ee, v138
	v_fmamk_f32 v87, v87, 0x3e0293ee, v138
	v_fmamk_f32 v88, v88, 0x3e0293ee, v138
	v_fmamk_f32 v89, v89, 0x3e0293ee, v138
	v_fmamk_f32 v90, v90, 0x3e0293ee, v138
	v_fmamk_f32 v91, v91, 0x3e0293ee, v138
	v_fmamk_f32 v92, v92, 0x3e0293ee, v138
	v_fmamk_f32 v93, v93, 0x3e0293ee, v138
	v_fmamk_f32 v94, v94, 0x3e0293ee, v138
	v_fmamk_f32 v95, v95, 0x3e0293ee, v138
	v_fmamk_f32 v96, v96, 0x3e0293ee, v138
	v_fmamk_f32 v97, v97, 0x3e0293ee, v138
	v_fmamk_f32 v139, v66, 0x3e0293ee, v138
	v_fmamk_f32 v140, v68, 0x3e0293ee, v138
	v_fmamk_f32 v141, v70, 0x3e0293ee, v138
	v_fmamk_f32 v142, v72, 0x3e0293ee, v138
	v_fmamk_f32 v143, v74, 0x3e0293ee, v138
	v_fmamk_f32 v144, v76, 0x3e0293ee, v138
	v_fmamk_f32 v145, v78, 0x3e0293ee, v138
	v_fmamk_f32 v146, v80, 0x3e0293ee, v138
	v_fmamk_f32 v181, v67, 0x3e0293ee, v138
	v_fmamk_f32 v182, v69, 0x3e0293ee, v138
	v_fmamk_f32 v188, v71, 0x3e0293ee, v138
	v_fmamk_f32 v189, v73, 0x3e0293ee, v138
	v_fmamk_f32 v190, v75, 0x3e0293ee, v138
	v_fmamk_f32 v191, v77, 0x3e0293ee, v138
	v_fmamk_f32 v192, v79, 0x3e0293ee, v138
	v_fmac_f32_e32 v138, 0x3e0293ee, v81
	v_exp_f32_e32 v147, v82
	v_exp_f32_e32 v148, v83
	v_exp_f32_e32 v149, v84
	v_exp_f32_e32 v150, v85
	v_exp_f32_e32 v151, v86
	v_exp_f32_e32 v152, v87
	v_exp_f32_e32 v153, v88
	v_exp_f32_e32 v154, v89
	v_exp_f32_e32 v155, v90
	v_exp_f32_e32 v156, v91
	v_exp_f32_e32 v157, v92
	v_exp_f32_e32 v183, v93
	v_exp_f32_e32 v184, v94
	v_exp_f32_e32 v185, v95
	v_exp_f32_e32 v186, v96
	v_exp_f32_e32 v187, v97
	s_waitcnt lgkmcnt(0)
	s_barrier
	ds_read_b128 v[66:69], v162
	ds_read_b128 v[70:73], v162 offset:8192
	ds_read_b128 v[130:133], v164
	ds_read_b128 v[134:137], v164 offset:8192
	v_exp_f32_e32 v138, v138
	s_waitcnt lgkmcnt(3)
	v_mfma_f32_32x32x16_bf16 v[82:97], v[66:69], v[98:101], 0
	s_waitcnt lgkmcnt(2)
	v_mfma_f32_32x32x16_bf16 v[66:81], v[70:73], v[98:101], 0
	s_waitcnt lgkmcnt(1)
	v_mfma_f32_32x32x16_bf16 v[82:97], v[130:133], v[102:105], v[82:97]
	s_waitcnt lgkmcnt(0)
	v_mfma_f32_32x32x16_bf16 v[66:81], v[134:137], v[102:105], v[66:81]
	ds_read_b128 v[130:133], v166
	ds_read_b128 v[134:137], v166 offset:8192
	s_waitcnt lgkmcnt(1)
	v_mfma_f32_32x32x16_bf16 v[82:97], v[130:133], v[106:109], v[82:97]
	s_waitcnt lgkmcnt(0)
	v_mfma_f32_32x32x16_bf16 v[66:81], v[134:137], v[106:109], v[66:81]
	ds_read_b128 v[130:133], v168
	ds_read_b128 v[134:137], v168 offset:8192
	s_waitcnt lgkmcnt(1)
	v_mfma_f32_32x32x16_bf16 v[82:97], v[130:133], v[110:113], v[82:97]
	s_waitcnt lgkmcnt(0)
	v_mfma_f32_32x32x16_bf16 v[66:81], v[134:137], v[110:113], v[66:81]
	ds_read_b128 v[130:133], v162 offset:128
	ds_read_b128 v[134:137], v162 offset:8320
	s_waitcnt lgkmcnt(1)
	v_mfma_f32_32x32x16_bf16 v[82:97], v[130:133], v[114:117], v[82:97]
	s_waitcnt lgkmcnt(0)
	v_mfma_f32_32x32x16_bf16 v[66:81], v[134:137], v[114:117], v[66:81]
	ds_read_b128 v[130:133], v164 offset:128
	ds_read_b128 v[134:137], v164 offset:8320
	s_waitcnt lgkmcnt(1)
	v_mfma_f32_32x32x16_bf16 v[82:97], v[130:133], v[118:121], v[82:97]
	s_waitcnt lgkmcnt(0)
	v_mfma_f32_32x32x16_bf16 v[66:81], v[134:137], v[118:121], v[66:81]
	ds_read_b128 v[130:133], v166 offset:128
	ds_read_b128 v[134:137], v166 offset:8320
	s_waitcnt lgkmcnt(1)
	v_mfma_f32_32x32x16_bf16 v[82:97], v[130:133], v[122:125], v[82:97]
	s_waitcnt lgkmcnt(0)
	v_mfma_f32_32x32x16_bf16 v[66:81], v[134:137], v[122:125], v[66:81]
	ds_read_b128 v[130:133], v168 offset:128
	ds_read_b128 v[134:137], v168 offset:8320
	s_waitcnt lgkmcnt(1)
	v_mfma_f32_32x32x16_bf16 v[82:97], v[130:133], v[126:129], v[82:97]
	v_exp_f32_e32 v130, v139
	v_exp_f32_e32 v139, v143
	v_exp_f32_e32 v143, v145
	v_exp_f32_e32 v145, v146
	v_add_f32_e32 v146, 0, v147
	v_add_f32_e32 v146, v148, v146
	v_add_f32_e32 v146, v149, v146
	v_add_f32_e32 v146, v150, v146
	v_add_f32_e32 v146, v151, v146
	v_add_f32_e32 v146, v152, v146
	v_add_f32_e32 v146, v153, v146
	v_add_f32_e32 v146, v154, v146
	v_add_f32_e32 v146, v155, v146
	v_add_f32_e32 v146, v156, v146
	v_add_f32_e32 v146, v157, v146
	v_add_f32_e32 v146, v183, v146
	v_add_f32_e32 v146, v184, v146
	v_exp_f32_e32 v131, v181
	v_add_f32_e32 v146, v185, v146
	v_exp_f32_e32 v132, v140
	v_add_f32_e32 v146, v186, v146
	v_exp_f32_e32 v133, v182
	v_add_f32_e32 v146, v187, v146
	s_waitcnt lgkmcnt(0)
; #define LAS __attribute__((address_space(3)))
; __device__ __forceinline__ void finishSM(f32x16& p0, f32x16& p1, float alpha, float& l_reg, bf16x8& pa0, bf16x8& pa1, bf16x8& pa2, bf16x8& pa3) {
; #pragma unroll
;     for (int r = 0; r < 16; ++r) p1[r] = __builtin_amdgcn_exp2f(p1[r]);
;     float ps = 0;
; #pragma unroll
;     for (int r = 0; r < 16; ++r) ps += p0[r];
; #pragma unroll
;     for (int r = 0; r < 16; ++r) ps += p1[r];
;     { auto rr = __builtin_amdgcn_permlane32_swap(__float_as_uint(ps), __float_as_uint(ps), false, false);
;       ps = __uint_as_float(rr[0]) + __uint_as_float(rr[1]); }
;     l_reg = l_reg * alpha + ps;
;     ...
;     PK4(p0, 0, pa0); PK4(p0, 8, pa1); PK4(p1, 0, pa2); PK4(p1, 8, pa3);
;     ...
; }
; template <int KB>
; __device__ __forceinline__ void qkt(f32x16& p0, f32x16& p1, const LAS char* K_lds, int r32, int hi, const bf16x8* qr) {
;     p0 = f32x16{}; p1 = f32x16{};
;     const LAS char* kb[4];
; #pragma unroll
;     for (int dd = 0; dd < 4; ++dd) kb[dd] = K_lds + KB * SHM_K + KSWZ(r32, (dd * 16 + hi * 8) * 2);
; #pragma unroll
;     for (int d0 = 0; d0 < 8; ++d0) { const LAS char* a = kb[d0 & 3] + (d0 >> 2) * 128;
;         bf16x8 b0 = *(const LAS bf16x8*)(a);
;         bf16x8 b1 = *(const LAS bf16x8*)(a + 32 * 256);
;         p0 = __builtin_amdgcn_mfma_f32_32x32x16_bf16(b0, qr[d0], p0, 0, 0, 0);
;         p1 = __builtin_amdgcn_mfma_f32_32x32x16_bf16(b1, qr[d0], p1, 0, 0, 0); }
; }
; template <int VB>
; __device__ __forceinline__ void pv_tile(f32x16* o, int vb0, bf16x8 pa0, bf16x8 pa1, bf16x8 pa2, bf16x8 pa3) {
;     ...
;     PV_D0(0); PV_D0(1); PV_D0(2); PV_D0(3);
	v_mfma_f32_32x32x16_bf16 v[66:81], v[134:137], v[126:129], v[66:81]
	v_exp_f32_e32 v134, v141
	v_add_f32_e32 v146, v130, v146
	v_exp_f32_e32 v135, v188
	v_add_f32_e32 v146, v131, v146
	v_exp_f32_e32 v136, v142
	v_add_f32_e32 v146, v132, v146
	v_exp_f32_e32 v137, v189
	v_add_f32_e32 v146, v133, v146
	v_add_f32_e32 v146, v134, v146
	v_exp_f32_e32 v140, v190
	v_add_f32_e32 v146, v135, v146
	v_exp_f32_e32 v141, v144
	v_add_f32_e32 v146, v136, v146
	v_exp_f32_e32 v142, v191
	v_add_f32_e32 v146, v137, v146
	v_add_f32_e32 v146, v139, v146
	v_exp_f32_e32 v144, v192
	v_add_f32_e32 v146, v140, v146
	v_add_f32_e32 v146, v141, v146
	v_add_f32_e32 v146, v142, v146
	v_add_f32_e32 v146, v143, v146
	v_add_f32_e32 v146, v144, v146
	v_add_f32_e32 v146, v145, v146
	v_add_f32_e32 v181, v138, v146
	v_mov_b32_e32 v182, v181
	s_nop 1
	v_permlane32_swap_b32_e32 v181, v182
	v_cvt_pk_bf16_f32 v146, v147, v148
	v_cvt_pk_bf16_f32 v147, v149, v150
	v_cvt_pk_bf16_f32 v148, v151, v152
	v_cvt_pk_bf16_f32 v149, v153, v154
	v_cvt_pk_bf16_f32 v150, v155, v156
	v_cvt_pk_bf16_f32 v151, v157, v183
	v_cvt_pk_bf16_f32 v152, v184, v185
	v_cvt_pk_bf16_f32 v153, v186, v187
	v_cvt_pk_bf16_f32 v154, v130, v131
	v_cvt_pk_bf16_f32 v155, v132, v133
	v_cvt_pk_bf16_f32 v156, v134, v135
	v_cvt_pk_bf16_f32 v157, v136, v137
	v_cvt_pk_bf16_f32 v184, v139, v140
	v_cvt_pk_bf16_f32 v185, v141, v142
	v_cvt_pk_bf16_f32 v186, v143, v144
	v_cvt_pk_bf16_f32 v187, v145, v138
	v_permlane32_swap_b32_e32 v146, v148
	v_permlane32_swap_b32_e32 v147, v149
	v_permlane32_swap_b32_e32 v150, v152
	v_permlane32_swap_b32_e32 v151, v153
	v_permlane32_swap_b32_e32 v154, v156
	v_permlane32_swap_b32_e32 v155, v157
	v_permlane32_swap_b32_e32 v184, v186
	v_permlane32_swap_b32_e32 v185, v187
	s_mov_b32 s4, 0x10000
	v_add_co_u32_e32 v130, vcc, s4, v158
	s_mov_b32 s4, 0x18000
	s_nop 0
	v_addc_co_u32_e32 v131, vcc, 0, v159, vcc
	v_add_co_u32_e32 v134, vcc, s4, v158
	s_mov_b32 s4, 0x20000
	s_nop 0
	v_addc_co_u32_e32 v135, vcc, 0, v159, vcc
	v_add_co_u32_e32 v138, vcc, s4, v158
	s_mov_b32 s4, 0x28000
	s_nop 0
	v_addc_co_u32_e32 v139, vcc, 0, v159, vcc
	v_add_co_u32_e32 v142, vcc, s4, v158
	global_load_dwordx4 v[130:133], v[130:131], off
	s_nop 0
	global_load_dwordx4 v[134:137], v[134:135], off
	v_addc_co_u32_e32 v143, vcc, 0, v159, vcc
	global_load_dwordx4 v[138:141], v[138:139], off
	s_nop 0
	global_load_dwordx4 v[142:145], v[142:143], off
	ds_write_b128 v0, v[146:149] offset:16384
	ds_write_b128 v0, v[150:153] offset:16400
	ds_write_b128 v0, v[154:157] offset:16416
	ds_write_b128 v0, v[184:187] offset:16432
	ds_read_b64_tr_b16 v[188:189], v169 offset:0x4000
	ds_read_b64_tr_b16 v[190:191], v169 offset:0x4800
	ds_read_b64_tr_b16 v[192:193], v169 offset:0x5000
	ds_read_b64_tr_b16 v[194:195], v169 offset:0x5800
	ds_read_b64_tr_b16 v[198:199], v169 offset:0x6000
	ds_read_b64_tr_b16 v[200:201], v169 offset:0x6800
	ds_read_b64_tr_b16 v[202:203], v169 offset:0x7000
	ds_read_b64_tr_b16 v[204:205], v169 offset:0x7800
	s_nop 0
	s_nop 0
	s_waitcnt lgkmcnt(6)
	v_mfma_f32_32x32x16_bf16 v[50:65], v[146:149], v[188:191], v[50:65]
	ds_read_b64_tr_b16 v[188:189], v169 offset:0x4200
	ds_read_b64_tr_b16 v[190:191], v169 offset:0x4a00
	s_waitcnt lgkmcnt(6)
	v_mfma_f32_32x32x16_bf16 v[50:65], v[150:153], v[192:195], v[50:65]
	ds_read_b64_tr_b16 v[192:193], v169 offset:0x5200
	ds_read_b64_tr_b16 v[194:195], v169 offset:0x5a00
	s_waitcnt lgkmcnt(6)
	v_mfma_f32_32x32x16_bf16 v[50:65], v[154:157], v[198:201], v[50:65]
	ds_read_b64_tr_b16 v[198:199], v169 offset:0x6200
	ds_read_b64_tr_b16 v[200:201], v169 offset:0x6a00
	s_waitcnt lgkmcnt(6)
	v_mfma_f32_32x32x16_bf16 v[50:65], v[184:187], v[202:205], v[50:65]
	ds_read_b64_tr_b16 v[202:203], v169 offset:0x7200
	ds_read_b64_tr_b16 v[204:205], v169 offset:0x7a00
	s_nop 0
	s_waitcnt lgkmcnt(6)
	v_mfma_f32_32x32x16_bf16 v[34:49], v[146:149], v[188:191], v[34:49]
	ds_read_b64_tr_b16 v[188:189], v169 offset:0x4400
	ds_read_b64_tr_b16 v[190:191], v169 offset:0x4c00
	s_waitcnt lgkmcnt(6)
	v_mfma_f32_32x32x16_bf16 v[34:49], v[150:153], v[192:195], v[34:49]
	ds_read_b64_tr_b16 v[192:193], v169 offset:0x5400
	ds_read_b64_tr_b16 v[194:195], v169 offset:0x5c00
	s_waitcnt lgkmcnt(6)
	v_mfma_f32_32x32x16_bf16 v[34:49], v[154:157], v[198:201], v[34:49]
	ds_read_b64_tr_b16 v[198:199], v169 offset:0x6400
	ds_read_b64_tr_b16 v[200:201], v169 offset:0x6c00
	s_waitcnt lgkmcnt(6)
	v_mfma_f32_32x32x16_bf16 v[34:49], v[184:187], v[202:205], v[34:49]
	ds_read_b64_tr_b16 v[202:203], v169 offset:0x7400
	ds_read_b64_tr_b16 v[204:205], v169 offset:0x7c00
	s_nop 0
	s_waitcnt lgkmcnt(6)
	v_mfma_f32_32x32x16_bf16 v[18:33], v[146:149], v[188:191], v[18:33]
	ds_read_b64_tr_b16 v[188:189], v169 offset:0x4600
	ds_read_b64_tr_b16 v[190:191], v169 offset:0x4e00
	s_waitcnt lgkmcnt(6)
	v_mfma_f32_32x32x16_bf16 v[18:33], v[150:153], v[192:195], v[18:33]
	ds_read_b64_tr_b16 v[192:193], v169 offset:0x5600
	ds_read_b64_tr_b16 v[194:195], v169 offset:0x5e00
	s_waitcnt lgkmcnt(6)
	v_mfma_f32_32x32x16_bf16 v[18:33], v[154:157], v[198:201], v[18:33]
	ds_read_b64_tr_b16 v[198:199], v169 offset:0x6600
	ds_read_b64_tr_b16 v[200:201], v169 offset:0x6e00
	s_waitcnt lgkmcnt(6)
	v_mfma_f32_32x32x16_bf16 v[18:33], v[184:187], v[202:205], v[18:33]
	ds_read_b64_tr_b16 v[202:203], v169 offset:0x7600
	ds_read_b64_tr_b16 v[204:205], v169 offset:0x7e00
	s_nop 0
	s_waitcnt lgkmcnt(6)
	v_mfma_f32_32x32x16_bf16 v[2:17], v[146:149], v[188:191], v[2:17]
	s_add_i32 s4, s79, 64
	s_cmp_le_u32 s4, s68
	s_waitcnt lgkmcnt(4)
	v_mfma_f32_32x32x16_bf16 v[2:17], v[150:153], v[192:195], v[2:17]
	s_waitcnt lgkmcnt(2)
	v_mfma_f32_32x32x16_bf16 v[2:17], v[154:157], v[198:201], v[2:17]
	s_waitcnt lgkmcnt(0)
	v_mfma_f32_32x32x16_bf16 v[2:17], v[184:187], v[202:205], v[2:17]
	s_cbranch_scc1 .LBB0_1304
; __device__ __forceinline__ void mask_tile(f32x16& p0, f32x16& p1, int dq) {
;     const float NEG = -__builtin_inff();
; #pragma unroll
;     for (int r = 0; r < 16; ++r) { const int c = (r & 3) + 8 * (r >> 2); if (dq - c < 0) p0[r] = NEG; if (dq - c - 32 < 0) p1[r] = NEG; }
; }
	v_subrev_u32_e32 v146, 64, v174
	v_cmp_gt_i32_e64 s[62:63], 26, v146
	v_cmp_gt_i32_e64 s[64:65], 27, v146
	v_cmp_gt_i32_e64 s[60:61], 25, v146
	s_and_b64 s[62:63], s[64:65], s[62:63]
	v_cmp_gt_i32_e64 s[58:59], 24, v146
	s_and_b64 s[60:61], s[62:63], s[60:61]
	v_cmp_gt_i32_e64 s[56:57], 19, v146
	s_and_b64 s[58:59], s[60:61], s[58:59]
	v_cmp_gt_i32_e64 s[54:55], 18, v146
	s_and_b64 s[56:57], s[58:59], s[56:57]
	v_cmp_gt_i32_e64 s[52:53], 17, v146
	s_and_b64 s[54:55], s[56:57], s[54:55]
	v_cmp_gt_i32_e64 s[50:51], 16, v146
	s_and_b64 s[52:53], s[54:55], s[52:53]
	v_cmp_gt_i32_e64 s[48:49], 11, v146
	s_and_b64 s[50:51], s[52:53], s[50:51]
	v_cmp_gt_i32_e64 s[46:47], 10, v146
	s_and_b64 s[48:49], s[50:51], s[48:49]
	v_cmp_gt_i32_e64 s[44:45], 9, v146
	s_and_b64 s[46:47], s[48:49], s[46:47]
	v_cmp_gt_i32_e64 s[42:43], 8, v146
	s_and_b64 s[44:45], s[46:47], s[44:45]
	v_cmp_gt_i32_e64 s[40:41], 3, v146
	s_and_b64 s[42:43], s[44:45], s[42:43]
	v_cmp_gt_i32_e64 s[38:39], 2, v146
	s_and_b64 s[40:41], s[42:43], s[40:41]
	v_cmp_gt_i32_e64 s[36:37], 1, v146
	s_and_b64 s[38:39], s[40:41], s[38:39]
	v_cmp_gt_i32_e64 s[34:35], 0, v146
	s_and_b64 s[36:37], s[38:39], s[36:37]
	s_and_b64 s[34:35], s[36:37], s[34:35]
	v_cmp_gt_i32_e64 s[30:31], 58, v146
	v_cndmask_b32_e64 v82, v82, v197, s[34:35]
	v_cmp_gt_i32_e64 s[34:35], 59, v146
	v_cmp_gt_i32_e64 s[28:29], 57, v146
	s_and_b64 s[30:31], s[34:35], s[30:31]
	v_cmp_gt_i32_e64 s[26:27], 56, v146
	s_and_b64 s[28:29], s[30:31], s[28:29]
	v_cmp_gt_i32_e64 s[24:25], 51, v146
	s_and_b64 s[26:27], s[28:29], s[26:27]
	v_cmp_gt_i32_e64 s[22:23], 50, v146
	s_and_b64 s[24:25], s[26:27], s[24:25]
	v_cmp_gt_i32_e64 s[20:21], 49, v146
	s_and_b64 s[22:23], s[24:25], s[22:23]
	v_cmp_gt_i32_e64 s[18:19], 48, v146
	s_and_b64 s[20:21], s[22:23], s[20:21]
	v_cmp_gt_i32_e64 s[16:17], 43, v146
	s_and_b64 s[18:19], s[20:21], s[18:19]
	v_cmp_gt_i32_e64 s[14:15], 42, v146
	s_and_b64 s[16:17], s[18:19], s[16:17]
	v_cmp_gt_i32_e64 s[12:13], 41, v146
	s_and_b64 s[14:15], s[16:17], s[14:15]
	v_cmp_gt_i32_e64 s[10:11], 40, v146
	s_and_b64 s[12:13], s[14:15], s[12:13]
	v_cmp_gt_i32_e64 s[8:9], 35, v146
	s_and_b64 s[10:11], s[12:13], s[10:11]
	v_cmp_gt_i32_e64 s[6:7], 34, v146
	s_and_b64 s[8:9], s[10:11], s[8:9]
	v_cmp_gt_i32_e64 s[4:5], 33, v146
	s_and_b64 s[6:7], s[8:9], s[6:7]
	v_cmp_gt_i32_e32 vcc, 32, v146
	s_and_b64 s[4:5], s[6:7], s[4:5]
	s_and_b64 vcc, s[4:5], vcc
	v_cndmask_b32_e64 v97, v97, v197, s[64:65]
	v_cndmask_b32_e64 v96, v96, v197, s[62:63]
	v_cndmask_b32_e64 v95, v95, v197, s[60:61]
	v_cndmask_b32_e64 v94, v94, v197, s[58:59]
	v_cndmask_b32_e64 v93, v93, v197, s[56:57]
	v_cndmask_b32_e64 v92, v92, v197, s[54:55]
	v_cndmask_b32_e64 v91, v91, v197, s[52:53]
	v_cndmask_b32_e64 v90, v90, v197, s[50:51]
	v_cndmask_b32_e64 v89, v89, v197, s[48:49]
	v_cndmask_b32_e64 v88, v88, v197, s[46:47]
	v_cndmask_b32_e64 v87, v87, v197, s[44:45]
	v_cndmask_b32_e64 v86, v86, v197, s[42:43]
	v_cndmask_b32_e64 v85, v85, v197, s[40:41]
	v_cndmask_b32_e64 v84, v84, v197, s[38:39]
	v_cndmask_b32_e64 v83, v83, v197, s[36:37]
	v_cndmask_b32_e64 v81, v81, v197, s[34:35]
	v_cndmask_b32_e64 v80, v80, v197, s[30:31]
	v_cndmask_b32_e64 v79, v79, v197, s[28:29]
	v_cndmask_b32_e64 v78, v78, v197, s[26:27]
	v_cndmask_b32_e64 v77, v77, v197, s[24:25]
	v_cndmask_b32_e64 v76, v76, v197, s[22:23]
	v_cndmask_b32_e64 v75, v75, v197, s[20:21]
	v_cndmask_b32_e64 v74, v74, v197, s[18:19]
	v_cndmask_b32_e64 v73, v73, v197, s[16:17]
	v_cndmask_b32_e64 v72, v72, v197, s[14:15]
	v_cndmask_b32_e64 v71, v71, v197, s[12:13]
	v_cndmask_b32_e64 v70, v70, v197, s[10:11]
	v_cndmask_b32_e64 v69, v69, v197, s[8:9]
	v_cndmask_b32_e64 v68, v68, v197, s[6:7]
	v_cndmask_b32_e64 v67, v67, v197, s[4:5]
	v_cndmask_b32_e32 v66, v66, v197, vcc

; #define LAS __attribute__((address_space(3)))
; __device__ __forceinline__ void finishSM(f32x16& p0, f32x16& p1, float alpha, float& l_reg, bf16x8& pa0, bf16x8& pa1, bf16x8& pa2, bf16x8& pa3) {
; #pragma unroll
;     for (int r = 0; r < 16; ++r) p1[r] = __builtin_amdgcn_exp2f(p1[r]);
;     float ps = 0;
; #pragma unroll
;     for (int r = 0; r < 16; ++r) ps += p0[r];
; #pragma unroll
;     for (int r = 0; r < 16; ++r) ps += p1[r];
;     { auto rr = __builtin_amdgcn_permlane32_swap(__float_as_uint(ps), __float_as_uint(ps), false, false);
;       ps = __uint_as_float(rr[0]) + __uint_as_float(rr[1]); }
;     l_reg = l_reg * alpha + ps;
;     ...
;     PK4(p0, 0, pa0); PK4(p0, 8, pa1); PK4(p1, 0, pa2); PK4(p1, 8, pa3);
;     ...
; }
; template <int KB>
; __device__ __forceinline__ void qkt(f32x16& p0, f32x16& p1, const LAS char* K_lds, int r32, int hi, const bf16x8* qr) {
;     p0 = f32x16{}; p1 = f32x16{};
;     const LAS char* kb[4];
; #pragma unroll
;     for (int dd = 0; dd < 4; ++dd) kb[dd] = K_lds + KB * SHM_K + KSWZ(r32, (dd * 16 + hi * 8) * 2);
; #pragma unroll
;     for (int d0 = 0; d0 < 8; ++d0) { const LAS char* a = kb[d0 & 3] + (d0 >> 2) * 128;
;         bf16x8 b0 = *(const LAS bf16x8*)(a);
;         bf16x8 b1 = *(const LAS bf16x8*)(a + 32 * 256);
;         p0 = __builtin_amdgcn_mfma_f32_32x32x16_bf16(b0, qr[d0], p0, 0, 0, 0);
;         p1 = __builtin_amdgcn_mfma_f32_32x32x16_bf16(b1, qr[d0], p1, 0, 0, 0); }
; }
; template <int VB>
; __device__ __forceinline__ void pv_tile(f32x16* o, int vb0, bf16x8 pa0, bf16x8 pa1, bf16x8 pa2, bf16x8 pa3) {
;     ...
;     PV_D0(0); PV_D0(1); PV_D0(2); PV_D0(3);
.LBB0_1448:
	v_add_u32_e32 v153, s31, v162
	v_add_u32_e32 v0, -2, v153
	v_lshl_add_u64 v[66:67], v[0:1], 3, s[22:23]
	global_load_dwordx2 v[150:151], v[66:67], off
	ds_read_b128 v[66:69], v163 offset:49152
	ds_read_b128 v[82:85], v163 offset:57344
	ds_read_b128 v[190:193], v182 offset:49152
	ds_read_b128 v[198:201], v182 offset:57344
	v_exp_f32_e32 v0, v144
	s_waitcnt lgkmcnt(3)
	v_mfma_f32_32x32x16_bf16 v[66:81], v[66:69], v[98:101], 0
	v_exp_f32_e32 v144, v145
	v_add_f32_e32 v145, 0, v146
	v_add_f32_e32 v145, v147, v145
	v_add_f32_e32 v145, v148, v145
	v_add_f32_e32 v145, v170, v145
	v_add_f32_e32 v145, v171, v145
	v_add_f32_e32 v145, v173, v145
	s_waitcnt lgkmcnt(2)
	v_mfma_f32_32x32x16_bf16 v[82:97], v[82:85], v[98:101], 0
	v_add_f32_e32 v145, v149, v145
	v_add_f32_e32 v145, v172, v145
	v_add_f32_e32 v145, v154, v145
	v_add_f32_e32 v145, v156, v145
	v_add_f32_e32 v145, v157, v145
	v_add_f32_e32 v145, v160, v145
	v_add_f32_e32 v145, v155, v145
	s_waitcnt lgkmcnt(1)
	v_mfma_f32_32x32x16_bf16 v[66:81], v[190:193], v[102:105], v[66:81]
	v_add_f32_e32 v145, v158, v145
	v_exp_f32_e32 v142, v142
	v_add_f32_e32 v145, v159, v145
	v_exp_f32_e32 v143, v143
	v_add_f32_e32 v145, v161, v145
	v_exp_f32_e32 v138, v138
	v_add_f32_e32 v145, v0, v145
	s_waitcnt lgkmcnt(0)
	v_mfma_f32_32x32x16_bf16 v[82:97], v[198:201], v[102:105], v[82:97]
	ds_read_b128 v[190:193], v183 offset:49152
	ds_read_b128 v[198:201], v183 offset:57344
	v_exp_f32_e32 v139, v139
	v_add_f32_e32 v145, v144, v145
	v_exp_f32_e32 v134, v134
	v_add_f32_e32 v145, v142, v145
	v_exp_f32_e32 v135, v135
	v_add_f32_e32 v145, v143, v145
	s_waitcnt lgkmcnt(1)
	v_mfma_f32_32x32x16_bf16 v[66:81], v[190:193], v[106:109], v[66:81]
	v_exp_f32_e32 v130, v130
	v_add_f32_e32 v145, v138, v145
	v_exp_f32_e32 v131, v131
	v_add_f32_e32 v145, v139, v145
	v_exp_f32_e32 v140, v140
	v_add_f32_e32 v145, v134, v145
	v_exp_f32_e32 v141, v141
	s_waitcnt lgkmcnt(0)
	v_mfma_f32_32x32x16_bf16 v[82:97], v[198:201], v[106:109], v[82:97]
	ds_read_b128 v[190:193], v184 offset:49152
	ds_read_b128 v[198:201], v184 offset:57344
	v_add_f32_e32 v145, v135, v145
	v_exp_f32_e32 v136, v136
	v_add_f32_e32 v145, v130, v145
	v_exp_f32_e32 v137, v137
	v_add_f32_e32 v145, v131, v145
	v_exp_f32_e32 v132, v132
	s_waitcnt lgkmcnt(1)
	v_mfma_f32_32x32x16_bf16 v[66:81], v[190:193], v[110:113], v[66:81]
	v_add_f32_e32 v145, v140, v145
	v_exp_f32_e32 v133, v133
	v_add_f32_e32 v145, v141, v145
	v_add_f32_e32 v145, v136, v145
	v_add_f32_e32 v145, v137, v145
	v_add_f32_e32 v145, v132, v145
	v_cvt_pk_bf16_f32 v146, v146, v147
	s_waitcnt lgkmcnt(0)
	v_mfma_f32_32x32x16_bf16 v[82:97], v[198:201], v[110:113], v[82:97]
	ds_read_b128 v[190:193], v163 offset:49280
	ds_read_b128 v[198:201], v163 offset:57472
	v_cvt_pk_bf16_f32 v147, v148, v170
	v_cvt_pk_bf16_f32 v148, v171, v173
	v_cvt_pk_bf16_f32 v149, v149, v172
	v_cvt_pk_bf16_f32 v194, v138, v139
	v_permlane32_swap_b32_e32 v146, v148
	s_waitcnt lgkmcnt(1)
	v_mfma_f32_32x32x16_bf16 v[66:81], v[190:193], v[114:117], v[66:81]
	v_permlane32_swap_b32_e32 v147, v149
	v_cvt_pk_bf16_f32 v156, v154, v156
	v_cvt_pk_bf16_f32 v157, v157, v160
	v_cvt_pk_bf16_f32 v158, v155, v158
	v_cvt_pk_bf16_f32 v159, v159, v161
	v_cvt_pk_bf16_f32 v195, v134, v135
	s_waitcnt lgkmcnt(0)
	v_mfma_f32_32x32x16_bf16 v[82:97], v[198:201], v[114:117], v[82:97]
	ds_read_b128 v[190:193], v182 offset:49280
	ds_read_b128 v[198:201], v182 offset:57472
	v_permlane32_swap_b32_e32 v156, v158
	v_permlane32_swap_b32_e32 v157, v159
	s_waitcnt lgkmcnt(1)
	v_mfma_f32_32x32x16_bf16 v[66:81], v[190:193], v[118:121], v[66:81]
	s_waitcnt lgkmcnt(0)
	v_mfma_f32_32x32x16_bf16 v[82:97], v[198:201], v[118:121], v[82:97]
	ds_read_b128 v[190:193], v183 offset:49280
	ds_read_b128 v[198:201], v183 offset:57472
	s_waitcnt lgkmcnt(1)
	v_mfma_f32_32x32x16_bf16 v[66:81], v[190:193], v[122:125], v[66:81]
	s_waitcnt lgkmcnt(0)
	v_mfma_f32_32x32x16_bf16 v[82:97], v[198:201], v[122:125], v[82:97]
	ds_read_b128 v[190:193], v184 offset:49280
	ds_read_b128 v[198:201], v184 offset:57472
	s_waitcnt lgkmcnt(1)
	v_mfma_f32_32x32x16_bf16 v[66:81], v[190:193], v[126:129], v[66:81]
	v_add_f32_e32 v190, v133, v145
	v_mov_b32_e32 v191, v190
	v_cvt_pk_bf16_f32 v192, v0, v144
	s_nop 0
	v_permlane32_swap_b32_e32 v190, v191
	v_cvt_pk_bf16_f32 v193, v142, v143
	v_permlane32_swap_b32_e32 v192, v194
	s_waitcnt lgkmcnt(0)
	v_mfma_f32_32x32x16_bf16 v[82:97], v[198:201], v[126:129], v[82:97]
	v_cvt_pk_bf16_f32 v198, v130, v131
	v_cvt_pk_bf16_f32 v199, v140, v141
	v_cvt_pk_bf16_f32 v200, v136, v137
	v_cvt_pk_bf16_f32 v201, v132, v133
	v_permlane32_swap_b32_e32 v193, v195
	v_permlane32_swap_b32_e32 v198, v200
	v_permlane32_swap_b32_e32 v199, v201
	v_lshl_add_u64 v[172:173], v[168:169], 0, s[20:21]
	v_add_co_u32_e32 v130, vcc, s42, v172
	v_lshl_add_u64 v[170:171], v[168:169], 0, s[68:69]
	s_nop 0
	v_addc_co_u32_e32 v131, vcc, 0, v173, vcc
	v_add_co_u32_e32 v134, vcc, s43, v172
	s_nop 1
	v_addc_co_u32_e32 v135, vcc, 0, v173, vcc
	v_add_co_u32_e32 v138, vcc, s42, v170
	global_load_dwordx4 v[130:133], v[130:131], off
	s_nop 0
	global_load_dwordx4 v[134:137], v[134:135], off
	v_addc_co_u32_e32 v139, vcc, 0, v171, vcc
	v_add_co_u32_e32 v142, vcc, s43, v170
	s_nop 1
	v_addc_co_u32_e32 v143, vcc, 0, v171, vcc
	global_load_dwordx4 v[138:141], v[138:139], off
	s_nop 0
	global_load_dwordx4 v[142:145], v[142:143], off
	ds_read_b64_tr_b16 v[202:203], v178 offset:0
	ds_read_b64_tr_b16 v[204:205], v178 offset:0x800
	ds_read_b64_tr_b16 v[206:207], v178 offset:0x1000
	ds_read_b64_tr_b16 v[208:209], v178 offset:0x1800
	ds_read_b64_tr_b16 v[210:211], v178 offset:0x2000
	ds_read_b64_tr_b16 v[212:213], v178 offset:0x2800
	ds_read_b64_tr_b16 v[214:215], v178 offset:0x3000
	ds_read_b64_tr_b16 v[216:217], v178 offset:0x3800
	s_nop 0
	s_nop 0
	s_waitcnt lgkmcnt(6)
; __device__ __forceinline__ void mask_bits(f32x16& p0, f32x16& p1, unsigned long long w, int hi) {
;     const unsigned long long wsft = w >> (4 * hi); const int lo = (int)(unsigned)wsft, hb = (int)(unsigned)(wsft >> 32); const int NEGB = (int)0xFF800000u;
; #pragma unroll
;     for (int r = 0; r < 16; ++r) { const int c = (r & 3) + 8 * (r >> 2);
;         const int t0 = __builtin_amdgcn_sbfe(lo, c, 1), t1 = __builtin_amdgcn_sbfe(hb, c, 1);
;         p0[r] = __int_as_float((__float_as_int(p0[r]) & t0) | (~t0 & NEGB)); p1[r] = __int_as_float((__float_as_int(p1[r]) & t1) | (~t1 & NEGB)); }
; }
; __device__ __forceinline__ void partialSM(f32x16& p0, f32x16& p1, float& m_reg, float& mn, float& alpha) {
;     float pmax = p0[0];
; #pragma unroll
;     for (int r = 1; r < 16; ++r) pmax = fmaxf(pmax, p0[r]);
; #pragma unroll
;     for (int r = 0; r < 16; ++r) pmax = fmaxf(pmax, p1[r]);
;     { auto rr = __builtin_amdgcn_permlane32_swap(__float_as_uint(pmax), __float_as_uint(pmax), false, false);
;       pmax = fmaxf(__uint_as_float(rr[0]), __uint_as_float(rr[1])); }
;     constexpr float C2 = 1.4426950408889634f * SCALE;
;     if (__builtin_expect(__all((pmax - m_reg) * SCALE <= THR), 1)) { mn = m_reg; alpha = 1.f; }
;     else { mn = fmaxf(m_reg, pmax); alpha = __builtin_amdgcn_exp2f((m_reg - mn) * C2); m_reg = mn; }
; template <int VB>
; __device__ __forceinline__ void pv_tile(f32x16* o, int vb0, bf16x8 pa0, bf16x8 pa1, bf16x8 pa2, bf16x8 pa3) {
;     ...
;     PV_D0(0); PV_D0(1); PV_D0(2); PV_D0(3);
	v_mfma_f32_32x32x16_bf16 v[2:17], v[146:149], v[202:205], v[2:17]
	ds_read_b64_tr_b16 v[202:203], v178 offset:0x200
	ds_read_b64_tr_b16 v[204:205], v178 offset:0xa00
	s_waitcnt lgkmcnt(6)
	v_mfma_f32_32x32x16_bf16 v[2:17], v[156:159], v[206:209], v[2:17]
	ds_read_b64_tr_b16 v[206:207], v178 offset:0x1200
	ds_read_b64_tr_b16 v[208:209], v178 offset:0x1a00
	s_waitcnt lgkmcnt(6)
	v_mfma_f32_32x32x16_bf16 v[2:17], v[192:195], v[210:213], v[2:17]
	ds_read_b64_tr_b16 v[210:211], v178 offset:0x2200
	ds_read_b64_tr_b16 v[212:213], v178 offset:0x2a00
	s_waitcnt lgkmcnt(6)
	v_mfma_f32_32x32x16_bf16 v[2:17], v[198:201], v[214:217], v[2:17]
	ds_read_b64_tr_b16 v[214:215], v178 offset:0x3200
	ds_read_b64_tr_b16 v[216:217], v178 offset:0x3a00
	s_nop 0
	s_waitcnt lgkmcnt(6)
	v_mfma_f32_32x32x16_bf16 v[50:65], v[146:149], v[202:205], v[50:65]
	ds_read_b64_tr_b16 v[202:203], v178 offset:0x400
	ds_read_b64_tr_b16 v[204:205], v178 offset:0xc00
	s_waitcnt lgkmcnt(6)
	v_mfma_f32_32x32x16_bf16 v[50:65], v[156:159], v[206:209], v[50:65]
	ds_read_b64_tr_b16 v[206:207], v178 offset:0x1400
	ds_read_b64_tr_b16 v[208:209], v178 offset:0x1c00
	s_waitcnt lgkmcnt(6)
	v_mfma_f32_32x32x16_bf16 v[50:65], v[192:195], v[210:213], v[50:65]
	ds_read_b64_tr_b16 v[210:211], v178 offset:0x2400
	ds_read_b64_tr_b16 v[212:213], v178 offset:0x2c00
	s_waitcnt lgkmcnt(6)
	v_mfma_f32_32x32x16_bf16 v[50:65], v[198:201], v[214:217], v[50:65]
	ds_read_b64_tr_b16 v[214:215], v178 offset:0x3400
	ds_read_b64_tr_b16 v[216:217], v178 offset:0x3c00
	s_nop 0
	s_waitcnt lgkmcnt(6)
	v_mfma_f32_32x32x16_bf16 v[34:49], v[146:149], v[202:205], v[34:49]
	ds_read_b64_tr_b16 v[202:203], v178 offset:0x600
	ds_read_b64_tr_b16 v[204:205], v178 offset:0xe00
	s_waitcnt lgkmcnt(6)
	v_mfma_f32_32x32x16_bf16 v[34:49], v[156:159], v[206:209], v[34:49]
	ds_read_b64_tr_b16 v[206:207], v178 offset:0x1600
	ds_read_b64_tr_b16 v[208:209], v178 offset:0x1e00
	s_waitcnt lgkmcnt(6)
	v_mfma_f32_32x32x16_bf16 v[34:49], v[192:195], v[210:213], v[34:49]
	ds_read_b64_tr_b16 v[210:211], v178 offset:0x2600
	ds_read_b64_tr_b16 v[212:213], v178 offset:0x2e00
	s_waitcnt lgkmcnt(6)
	v_mfma_f32_32x32x16_bf16 v[34:49], v[198:201], v[214:217], v[34:49]
	ds_read_b64_tr_b16 v[214:215], v178 offset:0x3600
	ds_read_b64_tr_b16 v[216:217], v178 offset:0x3e00
	s_waitcnt lgkmcnt(0)
	s_waitcnt vmcnt(4)
	v_lshrrev_b64 v[150:151], v166, v[150:151]
	v_bfe_i32 v0, v150, 0, 1
	v_mfma_f32_32x32x16_bf16 v[18:33], v[146:149], v[202:205], v[18:33]
	v_bfe_i32 v147, v151, 0, 1
	v_bitop3_b32 v146, v66, s91, v0 bitop3:0xe4
	v_bfe_i32 v66, v150, 1, 1
	v_bitop3_b32 v0, v82, s91, v147 bitop3:0xe4
	v_bfe_i32 v147, v151, 1, 1
	v_bitop3_b32 v82, v67, s91, v66 bitop3:0xe4
	v_bfe_i32 v67, v150, 2, 1
	v_bitop3_b32 v66, v83, s91, v147 bitop3:0xe4
	v_bfe_i32 v147, v151, 2, 1
	v_bitop3_b32 v83, v68, s91, v67 bitop3:0xe4
	v_bfe_i32 v68, v150, 3, 1
	v_bitop3_b32 v67, v84, s91, v147 bitop3:0xe4
	v_bfe_i32 v147, v151, 3, 1
	v_bitop3_b32 v84, v69, s91, v68 bitop3:0xe4
	v_bfe_i32 v69, v150, 8, 1
	v_bitop3_b32 v68, v85, s91, v147 bitop3:0xe4
	v_bfe_i32 v147, v151, 8, 1
	v_bitop3_b32 v85, v70, s91, v69 bitop3:0xe4
	v_bfe_i32 v70, v150, 9, 1
	v_bitop3_b32 v69, v86, s91, v147 bitop3:0xe4
	v_bfe_i32 v86, v151, 9, 1
	v_bitop3_b32 v147, v71, s91, v70 bitop3:0xe4
	v_bfe_i32 v71, v150, 10, 1
	v_bitop3_b32 v70, v87, s91, v86 bitop3:0xe4
	v_bfe_i32 v86, v151, 10, 1
	v_bitop3_b32 v148, v72, s91, v71 bitop3:0xe4
	v_bfe_i32 v72, v150, 11, 1
	v_bitop3_b32 v71, v88, s91, v86 bitop3:0xe4
	v_bfe_i32 v86, v151, 11, 1
	v_bitop3_b32 v88, v73, s91, v72 bitop3:0xe4
	v_bfe_i32 v72, v150, 16, 1
	v_bitop3_b32 v73, v89, s91, v86 bitop3:0xe4
	v_bfe_i32 v86, v151, 16, 1
	v_bitop3_b32 v89, v74, s91, v72 bitop3:0xe4
	v_bfe_i32 v72, v150, 17, 1
	v_bfe_i32 v74, v151, 17, 1
	v_bitop3_b32 v86, v90, s91, v86 bitop3:0xe4
	v_bitop3_b32 v90, v75, s91, v72 bitop3:0xe4
	v_bitop3_b32 v87, v91, s91, v74 bitop3:0xe4
	v_bfe_i32 v72, v150, 18, 1
	v_bfe_i32 v74, v151, 18, 1
	v_bitop3_b32 v91, v76, s91, v72 bitop3:0xe4
	v_bitop3_b32 v76, v92, s91, v74 bitop3:0xe4
	v_bfe_i32 v72, v150, 19, 1
	v_bfe_i32 v74, v151, 19, 1
	v_bitop3_b32 v92, v77, s91, v72 bitop3:0xe4
	v_bitop3_b32 v77, v93, s91, v74 bitop3:0xe4
	v_bfe_i32 v72, v150, 24, 1
	v_bfe_i32 v74, v151, 24, 1
	v_bitop3_b32 v93, v78, s91, v72 bitop3:0xe4
	v_bitop3_b32 v78, v94, s91, v74 bitop3:0xe4
	v_bfe_i32 v72, v150, 25, 1
	v_bfe_i32 v74, v151, 25, 1
	v_bitop3_b32 v79, v79, s91, v72 bitop3:0xe4
	v_bitop3_b32 v72, v95, s91, v74 bitop3:0xe4
	v_bfe_i32 v74, v150, 26, 1
	v_bfe_i32 v75, v151, 26, 1
	v_bitop3_b32 v80, v80, s91, v74 bitop3:0xe4
	v_bitop3_b32 v74, v96, s91, v75 bitop3:0xe4
	v_bfe_i32 v75, v150, 27, 1
	v_bfe_i32 v94, v151, 27, 1
	v_bitop3_b32 v81, v81, s91, v75 bitop3:0xe4
	v_bitop3_b32 v75, v97, s91, v94 bitop3:0xe4
	v_max_f32_e32 v94, v82, v82
	v_max_f32_e32 v95, v146, v146
	v_max_f32_e32 v94, v95, v94
	v_max3_f32 v94, v94, v83, v84
	v_max3_f32 v94, v94, v85, v147
	v_max3_f32 v94, v94, v148, v88
	v_max3_f32 v94, v94, v89, v90
	v_max3_f32 v94, v94, v91, v92
	v_max3_f32 v94, v94, v93, v79
	v_max3_f32 v94, v94, v80, v81
	v_mfma_f32_32x32x16_bf16 v[18:33], v[156:159], v[206:209], v[18:33]
	v_max3_f32 v94, v94, v0, v66
	v_max3_f32 v94, v94, v67, v68
	v_max3_f32 v94, v94, v69, v70
	v_max3_f32 v94, v94, v71, v73
	v_max3_f32 v94, v94, v86, v87
	v_max3_f32 v94, v94, v76, v77
	v_max3_f32 v94, v94, v78, v72
	v_max3_f32 v94, v94, v74, v75
	v_mfma_f32_32x32x16_bf16 v[18:33], v[192:195], v[210:213], v[18:33]
	v_mov_b32_e32 v95, v94
	s_nop 1
	v_permlane32_swap_b32_e32 v94, v95
	v_max_f32_e32 v95, v95, v95
	v_max_f32_e32 v94, v94, v94
	v_max_f32_e32 v94, v94, v95
	v_sub_f32_e32 v95, v94, v152
	v_mul_f32_e32 v95, 0x3db504f3, v95
	v_cmp_ge_f32_e32 vcc, s92, v95
	v_max_f32_e32 v95, v152, v152
	v_max_f32_e32 v94, v95, v94
	v_mfma_f32_32x32x16_bf16 v[18:33], v[198:201], v[214:217], v[18:33]
	v_sub_f32_e32 v95, v152, v94
	v_mul_f32_e32 v95, 0x3e0293ee, v95
	v_exp_f32_e32 v95, v95
	s_cmp_eq_u64 vcc, exec
	s_cselect_b64 s[2:3], -1, 0
	s_barrier
; #define SBAR() __builtin_amdgcn_sched_barrier(0)
; #define VMW() asm volatile("s_waitcnt vmcnt(0)" ::: "memory")
; #define SWRITE_HV(bf) do { *(LAS bf16x8*)(V_lds + (bf) * SHM_V + vst0) = S.st_v0; *(LAS bf16x8*)(V_lds + (bf) * SHM_V + vst0 + 8192) = S.st_v1; } while (0)
; #define SWRITE_H(bf) do { SWRITE_HV(bf); SWRITE_HK(bf); } while (0)
; #define MLOAD(t) do { mw = Mb[moff + (unsigned)(t)]; } while (0)
; #define MASKT(P0_, P1_, t) do { mask_bits(P0_, P1_, mw, hi); } while (0)
; #define VMW() asm volatile("s_waitcnt vmcnt(0)" ::: "memory")
; __device__ __forceinline__ void attn_block(const unsigned char* wsb, const BlockRef& cur, const BlockRef& nxt, int skv, LAS char* lds, Seam& S, int wave_) {
;     ...
;     f32x16 pA0, pA1, pB0, pB1; float mnA, mnB, alA, alB; bf16x8 pa0, pa1, pa2, pa3;
;     SWRITE_HV(0); SBAR();
;     MLOAD(0);
;     if (NT > 1) SLOAD_H(Kh, Vh, KBASE(1));
;     SBAR(); qkt<0>(pA0, pA1, K_lds, r32, hi, S.qr);
;     MASKT(pA0, pA1, 0); partialSM(pA0, pA1, m_reg, mnA, alA);
;     if (NT > 1) { VMW(); SWRITE_H(1); }
;     __syncthreads();
	s_waitcnt vmcnt(0)
	v_cndmask_b32_e64 v192, v95, 1.0, s[2:3]
	v_cmp_gt_f32_e32 vcc, 1.0, v192
	s_waitcnt vmcnt(3)
	ds_write_b128 v181, v[130:133]
	s_waitcnt vmcnt(2)
	ds_write_b128 v181, v[134:137] offset:8192
	s_waitcnt vmcnt(1)
	ds_write_b128 v187, v[138:141] offset:32768
	s_waitcnt vmcnt(0)
	ds_write_b128 v187, v[142:145] offset:40960
	s_cbranch_vccz .LBB0_1452
	s_and_saveexec_b64 s[24:25], s[0:1]
	ds_write_b32 v186, v192 offset:128
	s_or_b64 exec, exec, s[24:25]
	s_waitcnt lgkmcnt(0)
	ds_read_b128 v[154:157], v185 offset:224
	ds_read_b128 v[158:161], v185 offset:192
	ds_read_b128 v[198:201], v185 offset:160
	ds_read_b128 v[202:205], v185 offset:128
	s_waitcnt lgkmcnt(3)
	v_pk_mul_f32 v[16:17], v[16:17], v[156:157]
	s_waitcnt lgkmcnt(2)
	v_pk_mul_f32 v[12:13], v[12:13], v[160:161]
	s_waitcnt lgkmcnt(1)
	v_pk_mul_f32 v[8:9], v[8:9], v[200:201]
	s_waitcnt lgkmcnt(0)
	v_pk_mul_f32 v[4:5], v[4:5], v[204:205]
	v_pk_mul_f32 v[14:15], v[14:15], v[154:155]
	v_pk_mul_f32 v[10:11], v[10:11], v[158:159]
	v_pk_mul_f32 v[6:7], v[6:7], v[198:199]
	v_pk_mul_f32 v[2:3], v[2:3], v[202:203]
	v_pk_mul_f32 v[64:65], v[64:65], v[156:157]
	v_pk_mul_f32 v[60:61], v[60:61], v[160:161]
	v_pk_mul_f32 v[56:57], v[56:57], v[200:201]
	v_pk_mul_f32 v[52:53], v[52:53], v[204:205]
	v_pk_mul_f32 v[62:63], v[62:63], v[154:155]
	v_pk_mul_f32 v[58:59], v[58:59], v[158:159]
	v_pk_mul_f32 v[54:55], v[54:55], v[198:199]
	v_pk_mul_f32 v[50:51], v[50:51], v[202:203]
	v_pk_mul_f32 v[48:49], v[48:49], v[156:157]
	v_pk_mul_f32 v[44:45], v[44:45], v[160:161]
	v_pk_mul_f32 v[40:41], v[40:41], v[200:201]
	v_pk_mul_f32 v[36:37], v[36:37], v[204:205]
	v_pk_mul_f32 v[46:47], v[46:47], v[154:155]
	v_pk_mul_f32 v[42:43], v[42:43], v[158:159]
	v_pk_mul_f32 v[38:39], v[38:39], v[198:199]
	v_pk_mul_f32 v[34:35], v[34:35], v[202:203]
	v_pk_mul_f32 v[32:33], v[32:33], v[156:157]
	v_pk_mul_f32 v[28:29], v[28:29], v[160:161]
	v_pk_mul_f32 v[24:25], v[24:25], v[200:201]
	v_pk_mul_f32 v[20:21], v[20:21], v[204:205]
	v_pk_mul_f32 v[30:31], v[30:31], v[154:155]
	v_pk_mul_f32 v[26:27], v[26:27], v[158:159]
	v_pk_mul_f32 v[22:23], v[22:23], v[198:199]
	v_pk_mul_f32 v[18:19], v[18:19], v[202:203]

; __device__ __forceinline__ void mask_bits(f32x16& p0, f32x16& p1, unsigned long long w, int hi) {
;     const unsigned long long wsft = w >> (4 * hi); const int lo = (int)(unsigned)wsft, hb = (int)(unsigned)(wsft >> 32); const int NEGB = (int)0xFF800000u;
; #pragma unroll
;     for (int r = 0; r < 16; ++r) { const int c = (r & 3) + 8 * (r >> 2);
;         const int t0 = __builtin_amdgcn_sbfe(lo, c, 1), t1 = __builtin_amdgcn_sbfe(hb, c, 1);
;         p0[r] = __int_as_float((__float_as_int(p0[r]) & t0) | (~t0 & NEGB)); p1[r] = __int_as_float((__float_as_int(p1[r]) & t1) | (~t1 & NEGB)); }
; }
; __device__ __forceinline__ void partialSM(f32x16& p0, f32x16& p1, float& m_reg, float& mn, float& alpha) {
;     float pmax = p0[0];
; #pragma unroll
;     for (int r = 1; r < 16; ++r) pmax = fmaxf(pmax, p0[r]);
; #pragma unroll
;     for (int r = 0; r < 16; ++r) pmax = fmaxf(pmax, p1[r]);
;     { auto rr = __builtin_amdgcn_permlane32_swap(__float_as_uint(pmax), __float_as_uint(pmax), false, false);
;       pmax = fmaxf(__uint_as_float(rr[0]), __uint_as_float(rr[1])); }
;     constexpr float C2 = 1.4426950408889634f * SCALE;
;     if (__builtin_expect(__all((pmax - m_reg) * SCALE <= THR), 1)) { mn = m_reg; alpha = 1.f; }
;     else { mn = fmaxf(m_reg, pmax); alpha = __builtin_amdgcn_exp2f((m_reg - mn) * C2); m_reg = mn; }
; template <int VB>
; __device__ __forceinline__ void pv_tile(f32x16* o, int vb0, bf16x8 pa0, bf16x8 pa1, bf16x8 pa2, bf16x8 pa3) {
;     ...
;     PV_D0(0); PV_D0(1); PV_D0(2); PV_D0(3);
.LBB0_1454:
	ds_read_b64_tr_b16 v[170:171], v178 offset:0x4000
	ds_read_b64_tr_b16 v[172:173], v178 offset:0x4800
	ds_read_b64_tr_b16 v[198:199], v178 offset:0x5000
	ds_read_b64_tr_b16 v[200:201], v178 offset:0x5800
	ds_read_b64_tr_b16 v[202:203], v178 offset:0x6000
	ds_read_b64_tr_b16 v[204:205], v178 offset:0x6800
	ds_read_b64_tr_b16 v[206:207], v178 offset:0x7000
	ds_read_b64_tr_b16 v[208:209], v178 offset:0x7800
	s_nop 0
	s_nop 0
	s_waitcnt lgkmcnt(6)
	v_mfma_f32_32x32x16_bf16 v[2:17], v[146:149], v[170:173], v[2:17]
	ds_read_b64_tr_b16 v[170:171], v178 offset:0x4200
	ds_read_b64_tr_b16 v[172:173], v178 offset:0x4a00
	s_waitcnt lgkmcnt(6)
	v_mfma_f32_32x32x16_bf16 v[2:17], v[150:153], v[198:201], v[2:17]
	ds_read_b64_tr_b16 v[198:199], v178 offset:0x5200
	ds_read_b64_tr_b16 v[200:201], v178 offset:0x5a00
	s_waitcnt lgkmcnt(6)
	v_mfma_f32_32x32x16_bf16 v[2:17], v[154:157], v[202:205], v[2:17]
	ds_read_b64_tr_b16 v[202:203], v178 offset:0x6200
	ds_read_b64_tr_b16 v[204:205], v178 offset:0x6a00
	s_waitcnt lgkmcnt(6)
	v_mfma_f32_32x32x16_bf16 v[2:17], v[158:161], v[206:209], v[2:17]
	ds_read_b64_tr_b16 v[206:207], v178 offset:0x7200
	ds_read_b64_tr_b16 v[208:209], v178 offset:0x7a00
	s_nop 0
	s_waitcnt lgkmcnt(6)
	v_mfma_f32_32x32x16_bf16 v[50:65], v[146:149], v[170:173], v[50:65]
	ds_read_b64_tr_b16 v[170:171], v178 offset:0x4400
	ds_read_b64_tr_b16 v[172:173], v178 offset:0x4c00
	s_waitcnt lgkmcnt(6)
	v_mfma_f32_32x32x16_bf16 v[50:65], v[150:153], v[198:201], v[50:65]
	ds_read_b64_tr_b16 v[198:199], v178 offset:0x5400
	ds_read_b64_tr_b16 v[200:201], v178 offset:0x5c00
	s_waitcnt lgkmcnt(6)
	v_mfma_f32_32x32x16_bf16 v[50:65], v[154:157], v[202:205], v[50:65]
	ds_read_b64_tr_b16 v[202:203], v178 offset:0x6400
	ds_read_b64_tr_b16 v[204:205], v178 offset:0x6c00
	s_waitcnt lgkmcnt(6)
	v_mfma_f32_32x32x16_bf16 v[50:65], v[158:161], v[206:209], v[50:65]
	ds_read_b64_tr_b16 v[206:207], v178 offset:0x7400
	ds_read_b64_tr_b16 v[208:209], v178 offset:0x7c00
	s_nop 0
	s_waitcnt lgkmcnt(6)
	v_mfma_f32_32x32x16_bf16 v[34:49], v[146:149], v[170:173], v[34:49]
	ds_read_b64_tr_b16 v[170:171], v178 offset:0x4600
	ds_read_b64_tr_b16 v[172:173], v178 offset:0x4e00
	s_waitcnt lgkmcnt(6)
	v_mfma_f32_32x32x16_bf16 v[34:49], v[150:153], v[198:201], v[34:49]
	ds_read_b64_tr_b16 v[198:199], v178 offset:0x5600
	ds_read_b64_tr_b16 v[200:201], v178 offset:0x5e00
	s_waitcnt lgkmcnt(6)
	v_mfma_f32_32x32x16_bf16 v[34:49], v[154:157], v[202:205], v[34:49]
	ds_read_b64_tr_b16 v[202:203], v178 offset:0x6600
	ds_read_b64_tr_b16 v[204:205], v178 offset:0x6e00
	s_waitcnt lgkmcnt(6)
	v_mfma_f32_32x32x16_bf16 v[34:49], v[158:161], v[206:209], v[34:49]
	ds_read_b64_tr_b16 v[206:207], v178 offset:0x7600
	ds_read_b64_tr_b16 v[208:209], v178 offset:0x7e00
	s_nop 0
	s_waitcnt lgkmcnt(6)
	v_mfma_f32_32x32x16_bf16 v[18:33], v[146:149], v[170:173], v[18:33]
	s_barrier
	v_mfma_f32_32x32x16_bf16 v[18:33], v[150:153], v[198:201], v[18:33]
	s_waitcnt vmcnt(4)
	v_lshrrev_b64 v[150:151], v166, v[174:175]
	v_bfe_i32 v146, v150, 0, 1
	v_bitop3_b32 v146, v82, s91, v146 bitop3:0xe4
	v_bfe_i32 v82, v150, 1, 1
	v_bitop3_b32 v147, v83, s91, v82 bitop3:0xe4
	v_bfe_i32 v82, v150, 2, 1
	v_bitop3_b32 v148, v84, s91, v82 bitop3:0xe4
	v_bfe_i32 v82, v150, 3, 1
	v_bitop3_b32 v85, v85, s91, v82 bitop3:0xe4
	v_bfe_i32 v82, v150, 8, 1
	v_bitop3_b32 v86, v86, s91, v82 bitop3:0xe4
	v_bfe_i32 v82, v150, 9, 1
	v_bitop3_b32 v87, v87, s91, v82 bitop3:0xe4
	v_bfe_i32 v82, v150, 10, 1
	v_bitop3_b32 v88, v88, s91, v82 bitop3:0xe4
	v_bfe_i32 v82, v150, 11, 1
	v_bitop3_b32 v89, v89, s91, v82 bitop3:0xe4
	v_bfe_i32 v82, v150, 16, 1
	v_bitop3_b32 v90, v90, s91, v82 bitop3:0xe4
	v_bfe_i32 v82, v150, 17, 1
	v_bitop3_b32 v91, v91, s91, v82 bitop3:0xe4
	v_bfe_i32 v82, v150, 18, 1
	v_bitop3_b32 v92, v92, s91, v82 bitop3:0xe4
	v_bfe_i32 v82, v150, 19, 1
	v_bitop3_b32 v93, v93, s91, v82 bitop3:0xe4
	v_bfe_i32 v82, v150, 24, 1
	v_bitop3_b32 v94, v94, s91, v82 bitop3:0xe4
	v_bfe_i32 v82, v150, 25, 1
	v_bitop3_b32 v95, v95, s91, v82 bitop3:0xe4
	v_bfe_i32 v82, v150, 26, 1
	v_bitop3_b32 v149, v96, s91, v82 bitop3:0xe4
	v_bfe_i32 v82, v150, 27, 1
	v_bfe_i32 v152, v151, 0, 1
	v_bfe_i32 v153, v151, 1, 1
	v_bitop3_b32 v96, v97, s91, v82 bitop3:0xe4
	v_max_f32_e32 v82, v147, v147
	v_max_f32_e32 v83, v146, v146
	v_max_f32_e32 v82, v83, v82
	v_bitop3_b32 v67, v67, s91, v153 bitop3:0xe4
	v_bitop3_b32 v66, v66, s91, v152 bitop3:0xe4
	v_max3_f32 v82, v82, v148, v85
	v_bfe_i32 v83, v151, 3, 1
	v_bfe_i32 v84, v151, 2, 1
	v_max3_f32 v82, v82, v86, v87
	v_max3_f32 v82, v82, v88, v89
	v_bitop3_b32 v69, v69, s91, v83 bitop3:0xe4
	v_bitop3_b32 v68, v68, s91, v84 bitop3:0xe4
	v_max3_f32 v82, v82, v90, v91
	v_bfe_i32 v83, v151, 9, 1
	v_bfe_i32 v84, v151, 8, 1
	v_max3_f32 v82, v82, v92, v93
	v_max3_f32 v82, v82, v94, v95
	v_bitop3_b32 v71, v71, s91, v83 bitop3:0xe4
	v_bitop3_b32 v70, v70, s91, v84 bitop3:0xe4
	v_max3_f32 v82, v82, v149, v96
	v_bfe_i32 v83, v151, 11, 1
	v_bfe_i32 v84, v151, 10, 1
	v_max3_f32 v82, v82, v66, v67
	v_max3_f32 v82, v82, v68, v69
	v_bitop3_b32 v73, v73, s91, v83 bitop3:0xe4
	v_bitop3_b32 v72, v72, s91, v84 bitop3:0xe4
	v_max3_f32 v82, v82, v70, v71
	v_max3_f32 v84, v82, v72, v73
	v_bfe_i32 v82, v151, 17, 1
	v_bfe_i32 v83, v151, 16, 1
	v_bitop3_b32 v75, v75, s91, v82 bitop3:0xe4
	v_bitop3_b32 v74, v74, s91, v83 bitop3:0xe4
	v_mov_b32_e32 v83, v75
	v_mov_b32_e32 v82, v74
	v_bfe_i32 v74, v151, 19, 1
	v_bfe_i32 v75, v151, 18, 1
	v_bitop3_b32 v74, v77, s91, v74 bitop3:0xe4
	v_bitop3_b32 v76, v76, s91, v75 bitop3:0xe4
	v_mov_b32_e32 v75, v74
	v_mov_b32_e32 v74, v76
	v_bfe_i32 v76, v151, 25, 1
	v_bfe_i32 v77, v151, 24, 1
	v_mfma_f32_32x32x16_bf16 v[18:33], v[154:157], v[202:205], v[18:33]
	v_bitop3_b32 v76, v79, s91, v76 bitop3:0xe4
	v_bitop3_b32 v78, v78, s91, v77 bitop3:0xe4
	v_mov_b32_e32 v77, v76
	v_mov_b32_e32 v76, v78
	v_bfe_i32 v78, v151, 27, 1
	v_bfe_i32 v79, v151, 26, 1
	v_max3_f32 v84, v84, v82, v83
	v_max3_f32 v84, v84, v74, v75
	v_bitop3_b32 v78, v81, s91, v78 bitop3:0xe4
	v_bitop3_b32 v80, v80, s91, v79 bitop3:0xe4
	v_max3_f32 v84, v84, v76, v77
	v_mov_b32_e32 v79, v78
	v_mov_b32_e32 v78, v80
	v_max3_f32 v80, v84, v78, v79
	v_mov_b32_e32 v81, v80
	v_mfma_f32_32x32x16_bf16 v[18:33], v[158:161], v[206:209], v[18:33]
	s_nop 0
	v_permlane32_swap_b32_e32 v80, v81
	v_max_f32_e32 v81, v81, v81
	v_max_f32_e32 v80, v80, v80
	v_max_f32_e32 v80, v80, v81
	v_sub_f32_e32 v81, v80, v193
	v_mul_f32_e32 v81, 0x3db504f3, v81
	v_cmp_ge_f32_e32 vcc, s92, v81
	s_cmp_eq_u64 vcc, exec
	s_cselect_b64 s[2:3], -1, 0
	s_andn2_b64 vcc, exec, s[24:25]
	s_cbranch_vccnz .LBB0_1456
	s_waitcnt vmcnt(0)
	ds_write_b128 v181, v[130:133] offset:16384
	ds_write_b128 v181, v[134:137] offset:24576
	ds_write_b128 v187, v[138:141] offset:49152
	ds_write_b128 v187, v[142:145] offset:57344

; template <int VB>
; __device__ __forceinline__ void pv_tile(f32x16* o, int vb0, bf16x8 pa0, bf16x8 pa1, bf16x8 pa2, bf16x8 pa3) {
;     ...
;     PV_D0(0); PV_D0(1); PV_D0(2); PV_D0(3);
.LBB0_1593:
	v_add_u32_e32 v153, s27, v162
	v_add_u32_e32 v0, -2, v153
	v_lshl_add_u64 v[66:67], v[0:1], 3, s[22:23]
	global_load_dwordx2 v[150:151], v[66:67], off
	ds_read_b128 v[66:69], v163 offset:49152
	ds_read_b128 v[82:85], v163 offset:57344
	ds_read_b128 v[190:193], v181 offset:49152
	ds_read_b128 v[198:201], v181 offset:57344
	v_exp_f32_e32 v0, v144
	s_waitcnt lgkmcnt(3)
	v_mfma_f32_32x32x16_bf16 v[66:81], v[66:69], v[98:101], 0
	v_exp_f32_e32 v144, v145
	v_add_f32_e32 v145, 0, v146
	v_add_f32_e32 v145, v147, v145
	v_add_f32_e32 v145, v148, v145
	v_add_f32_e32 v145, v170, v145
	v_add_f32_e32 v145, v171, v145
	v_add_f32_e32 v145, v173, v145
	s_waitcnt lgkmcnt(2)
	v_mfma_f32_32x32x16_bf16 v[82:97], v[82:85], v[98:101], 0
	v_add_f32_e32 v145, v149, v145
	v_add_f32_e32 v145, v172, v145
	v_add_f32_e32 v145, v154, v145
	v_add_f32_e32 v145, v156, v145
	v_add_f32_e32 v145, v157, v145
	v_add_f32_e32 v145, v160, v145
	v_add_f32_e32 v145, v155, v145
	s_waitcnt lgkmcnt(1)
	v_mfma_f32_32x32x16_bf16 v[66:81], v[190:193], v[102:105], v[66:81]
	v_add_f32_e32 v145, v158, v145
	v_exp_f32_e32 v142, v142
	v_add_f32_e32 v145, v159, v145
	v_exp_f32_e32 v143, v143
	v_add_f32_e32 v145, v161, v145
	v_exp_f32_e32 v138, v138
	v_add_f32_e32 v145, v0, v145
	s_waitcnt lgkmcnt(0)
	v_mfma_f32_32x32x16_bf16 v[82:97], v[198:201], v[102:105], v[82:97]
	ds_read_b128 v[190:193], v182 offset:49152
	ds_read_b128 v[198:201], v182 offset:57344
	v_exp_f32_e32 v139, v139
	v_add_f32_e32 v145, v144, v145
	v_exp_f32_e32 v134, v134
	v_add_f32_e32 v145, v142, v145
	v_exp_f32_e32 v135, v135
	v_add_f32_e32 v145, v143, v145
	s_waitcnt lgkmcnt(1)
	v_mfma_f32_32x32x16_bf16 v[66:81], v[190:193], v[106:109], v[66:81]
	v_exp_f32_e32 v130, v130
	v_add_f32_e32 v145, v138, v145
	v_exp_f32_e32 v131, v131
	v_add_f32_e32 v145, v139, v145
	v_exp_f32_e32 v140, v140
	v_add_f32_e32 v145, v134, v145
	v_exp_f32_e32 v141, v141
	s_waitcnt lgkmcnt(0)
	v_mfma_f32_32x32x16_bf16 v[82:97], v[198:201], v[106:109], v[82:97]
	ds_read_b128 v[190:193], v183 offset:49152
	ds_read_b128 v[198:201], v183 offset:57344
	v_add_f32_e32 v145, v135, v145
	v_exp_f32_e32 v136, v136
	v_add_f32_e32 v145, v130, v145
	v_exp_f32_e32 v137, v137
	v_add_f32_e32 v145, v131, v145
	v_exp_f32_e32 v132, v132
	s_waitcnt lgkmcnt(1)
	v_mfma_f32_32x32x16_bf16 v[66:81], v[190:193], v[110:113], v[66:81]
	v_add_f32_e32 v145, v140, v145
	v_exp_f32_e32 v133, v133
	v_add_f32_e32 v145, v141, v145
	v_add_f32_e32 v145, v136, v145
	v_add_f32_e32 v145, v137, v145
	v_add_f32_e32 v145, v132, v145
	v_add_f32_e32 v189, v133, v145
	s_waitcnt lgkmcnt(0)
	v_mfma_f32_32x32x16_bf16 v[82:97], v[198:201], v[110:113], v[82:97]
	ds_read_b128 v[190:193], v163 offset:49280
	ds_read_b128 v[198:201], v163 offset:57472
	v_cvt_pk_bf16_f32 v146, v146, v147
	v_cvt_pk_bf16_f32 v147, v148, v170
	v_cvt_pk_bf16_f32 v148, v171, v173
	v_cvt_pk_bf16_f32 v149, v149, v172
	s_nop 0
	v_permlane32_swap_b32_e32 v146, v148
	s_waitcnt lgkmcnt(1)
	v_mfma_f32_32x32x16_bf16 v[66:81], v[190:193], v[114:117], v[66:81]
	v_permlane32_swap_b32_e32 v147, v149
	v_cvt_pk_bf16_f32 v156, v154, v156
	v_cvt_pk_bf16_f32 v157, v157, v160
	v_cvt_pk_bf16_f32 v158, v155, v158
	v_cvt_pk_bf16_f32 v159, v159, v161
	v_cvt_pk_bf16_f32 v194, v138, v139
	s_waitcnt lgkmcnt(0)
	v_mfma_f32_32x32x16_bf16 v[82:97], v[198:201], v[114:117], v[82:97]
	ds_read_b128 v[190:193], v181 offset:49280
	ds_read_b128 v[198:201], v181 offset:57472
	v_cvt_pk_bf16_f32 v195, v134, v135
	v_permlane32_swap_b32_e32 v156, v158
	v_permlane32_swap_b32_e32 v157, v159
	s_waitcnt lgkmcnt(1)
	v_mfma_f32_32x32x16_bf16 v[66:81], v[190:193], v[118:121], v[66:81]
	s_waitcnt lgkmcnt(0)
	v_mfma_f32_32x32x16_bf16 v[82:97], v[198:201], v[118:121], v[82:97]
	ds_read_b128 v[190:193], v182 offset:49280
	ds_read_b128 v[198:201], v182 offset:57472
	s_waitcnt lgkmcnt(1)
	v_mfma_f32_32x32x16_bf16 v[66:81], v[190:193], v[122:125], v[66:81]
	s_waitcnt lgkmcnt(0)
	v_mfma_f32_32x32x16_bf16 v[82:97], v[198:201], v[122:125], v[82:97]
	ds_read_b128 v[190:193], v183 offset:49280
	ds_read_b128 v[198:201], v183 offset:57472
	s_waitcnt lgkmcnt(1)
	v_mfma_f32_32x32x16_bf16 v[66:81], v[190:193], v[126:129], v[66:81]
	v_mov_b32_e32 v190, v189
	s_nop 1
	v_permlane32_swap_b32_e32 v189, v190
	v_cvt_pk_bf16_f32 v192, v0, v144
	v_cvt_pk_bf16_f32 v193, v142, v143
	s_nop 0
	v_permlane32_swap_b32_e32 v192, v194
	s_waitcnt lgkmcnt(0)
	v_mfma_f32_32x32x16_bf16 v[82:97], v[198:201], v[126:129], v[82:97]
	v_cvt_pk_bf16_f32 v198, v130, v131
	v_cvt_pk_bf16_f32 v199, v140, v141
	v_cvt_pk_bf16_f32 v200, v136, v137
	v_cvt_pk_bf16_f32 v201, v132, v133
	v_permlane32_swap_b32_e32 v193, v195
	v_permlane32_swap_b32_e32 v198, v200
	v_permlane32_swap_b32_e32 v199, v201
	v_lshl_add_u64 v[172:173], v[168:169], 0, s[20:21]
	v_add_co_u32_e32 v130, vcc, s42, v172
	v_lshl_add_u64 v[170:171], v[168:169], 0, s[68:69]
	s_nop 0
	v_addc_co_u32_e32 v131, vcc, 0, v173, vcc
	v_add_co_u32_e32 v134, vcc, s43, v172
	s_nop 1
	v_addc_co_u32_e32 v135, vcc, 0, v173, vcc
	v_add_co_u32_e32 v138, vcc, s42, v170
	global_load_dwordx4 v[130:133], v[130:131], off
	s_nop 0
	global_load_dwordx4 v[134:137], v[134:135], off
	v_addc_co_u32_e32 v139, vcc, 0, v171, vcc
	v_add_co_u32_e32 v142, vcc, s43, v170
	s_nop 1
	v_addc_co_u32_e32 v143, vcc, 0, v171, vcc
	global_load_dwordx4 v[138:141], v[138:139], off
	s_nop 0
	global_load_dwordx4 v[142:145], v[142:143], off
	ds_read_b64_tr_b16 v[202:203], v178 offset:0
	ds_read_b64_tr_b16 v[204:205], v178 offset:0x800
	ds_read_b64_tr_b16 v[206:207], v178 offset:0x1000
	ds_read_b64_tr_b16 v[208:209], v178 offset:0x1800
	ds_read_b64_tr_b16 v[210:211], v178 offset:0x2000
	ds_read_b64_tr_b16 v[212:213], v178 offset:0x2800
	ds_read_b64_tr_b16 v[214:215], v178 offset:0x3000
	ds_read_b64_tr_b16 v[216:217], v178 offset:0x3800
	s_nop 0
	s_nop 0
	s_waitcnt lgkmcnt(6)
; __device__ __forceinline__ void mask_bits(f32x16& p0, f32x16& p1, unsigned long long w, int hi) {
;     const unsigned long long wsft = w >> (4 * hi); const int lo = (int)(unsigned)wsft, hb = (int)(unsigned)(wsft >> 32); const int NEGB = (int)0xFF800000u;
; #pragma unroll
;     for (int r = 0; r < 16; ++r) { const int c = (r & 3) + 8 * (r >> 2);
;         const int t0 = __builtin_amdgcn_sbfe(lo, c, 1), t1 = __builtin_amdgcn_sbfe(hb, c, 1);
;         p0[r] = __int_as_float((__float_as_int(p0[r]) & t0) | (~t0 & NEGB)); p1[r] = __int_as_float((__float_as_int(p1[r]) & t1) | (~t1 & NEGB)); }
; }
; __device__ __forceinline__ void partialSM(f32x16& p0, f32x16& p1, float& m_reg, float& mn, float& alpha) {
;     float pmax = p0[0];
; #pragma unroll
;     for (int r = 1; r < 16; ++r) pmax = fmaxf(pmax, p0[r]);
; #pragma unroll
;     for (int r = 0; r < 16; ++r) pmax = fmaxf(pmax, p1[r]);
;     { auto rr = __builtin_amdgcn_permlane32_swap(__float_as_uint(pmax), __float_as_uint(pmax), false, false);
;       pmax = fmaxf(__uint_as_float(rr[0]), __uint_as_float(rr[1])); }
;     constexpr float C2 = 1.4426950408889634f * SCALE;
;     if (__builtin_expect(__all((pmax - m_reg) * SCALE <= THR), 1)) { mn = m_reg; alpha = 1.f; }
;     else { mn = fmaxf(m_reg, pmax); alpha = __builtin_amdgcn_exp2f((m_reg - mn) * C2); m_reg = mn; }
; template <int VB>
; __device__ __forceinline__ void pv_tile(f32x16* o, int vb0, bf16x8 pa0, bf16x8 pa1, bf16x8 pa2, bf16x8 pa3) {
;     ...
;     PV_D0(0); PV_D0(1); PV_D0(2); PV_D0(3);
	v_mfma_f32_32x32x16_bf16 v[2:17], v[146:149], v[202:205], v[2:17]
	ds_read_b64_tr_b16 v[202:203], v178 offset:0x200
	ds_read_b64_tr_b16 v[204:205], v178 offset:0xa00
	s_waitcnt lgkmcnt(6)
	v_mfma_f32_32x32x16_bf16 v[2:17], v[156:159], v[206:209], v[2:17]
	ds_read_b64_tr_b16 v[206:207], v178 offset:0x1200
	ds_read_b64_tr_b16 v[208:209], v178 offset:0x1a00
	s_waitcnt lgkmcnt(6)
	v_mfma_f32_32x32x16_bf16 v[2:17], v[192:195], v[210:213], v[2:17]
	ds_read_b64_tr_b16 v[210:211], v178 offset:0x2200
	ds_read_b64_tr_b16 v[212:213], v178 offset:0x2a00
	s_waitcnt lgkmcnt(6)
	v_mfma_f32_32x32x16_bf16 v[2:17], v[198:201], v[214:217], v[2:17]
	ds_read_b64_tr_b16 v[214:215], v178 offset:0x3200
	ds_read_b64_tr_b16 v[216:217], v178 offset:0x3a00
	s_nop 0
	s_waitcnt lgkmcnt(6)
	v_mfma_f32_32x32x16_bf16 v[50:65], v[146:149], v[202:205], v[50:65]
	ds_read_b64_tr_b16 v[202:203], v178 offset:0x400
	ds_read_b64_tr_b16 v[204:205], v178 offset:0xc00
	s_waitcnt lgkmcnt(6)
	v_mfma_f32_32x32x16_bf16 v[50:65], v[156:159], v[206:209], v[50:65]
	ds_read_b64_tr_b16 v[206:207], v178 offset:0x1400
	ds_read_b64_tr_b16 v[208:209], v178 offset:0x1c00
	s_waitcnt lgkmcnt(6)
	v_mfma_f32_32x32x16_bf16 v[50:65], v[192:195], v[210:213], v[50:65]
	ds_read_b64_tr_b16 v[210:211], v178 offset:0x2400
	ds_read_b64_tr_b16 v[212:213], v178 offset:0x2c00
	s_waitcnt lgkmcnt(6)
	v_mfma_f32_32x32x16_bf16 v[50:65], v[198:201], v[214:217], v[50:65]
	ds_read_b64_tr_b16 v[214:215], v178 offset:0x3400
	ds_read_b64_tr_b16 v[216:217], v178 offset:0x3c00
	s_nop 0
	s_waitcnt lgkmcnt(6)
	v_mfma_f32_32x32x16_bf16 v[34:49], v[146:149], v[202:205], v[34:49]
	ds_read_b64_tr_b16 v[202:203], v178 offset:0x600
	ds_read_b64_tr_b16 v[204:205], v178 offset:0xe00
	s_waitcnt lgkmcnt(6)
	v_mfma_f32_32x32x16_bf16 v[34:49], v[156:159], v[206:209], v[34:49]
	ds_read_b64_tr_b16 v[206:207], v178 offset:0x1600
	ds_read_b64_tr_b16 v[208:209], v178 offset:0x1e00
	s_waitcnt lgkmcnt(6)
	v_mfma_f32_32x32x16_bf16 v[34:49], v[192:195], v[210:213], v[34:49]
	ds_read_b64_tr_b16 v[210:211], v178 offset:0x2600
	ds_read_b64_tr_b16 v[212:213], v178 offset:0x2e00
	s_waitcnt lgkmcnt(6)
	v_mfma_f32_32x32x16_bf16 v[34:49], v[198:201], v[214:217], v[34:49]
	ds_read_b64_tr_b16 v[214:215], v178 offset:0x3600
	ds_read_b64_tr_b16 v[216:217], v178 offset:0x3e00
	s_waitcnt lgkmcnt(0)
	s_waitcnt vmcnt(4)
	v_lshrrev_b64 v[150:151], v166, v[150:151]
	v_bfe_i32 v0, v150, 0, 1
	v_mfma_f32_32x32x16_bf16 v[18:33], v[146:149], v[202:205], v[18:33]
	v_bfe_i32 v147, v151, 0, 1
	v_bitop3_b32 v146, v66, s91, v0 bitop3:0xe4
	v_bfe_i32 v66, v150, 1, 1
	v_bitop3_b32 v0, v82, s91, v147 bitop3:0xe4
	v_bfe_i32 v147, v151, 1, 1
	v_bitop3_b32 v82, v67, s91, v66 bitop3:0xe4
	v_bfe_i32 v67, v150, 2, 1
	v_bitop3_b32 v66, v83, s91, v147 bitop3:0xe4
	v_bfe_i32 v147, v151, 2, 1
	v_bitop3_b32 v83, v68, s91, v67 bitop3:0xe4
	v_bfe_i32 v68, v150, 3, 1
	v_bitop3_b32 v67, v84, s91, v147 bitop3:0xe4
	v_bfe_i32 v147, v151, 3, 1
	v_bitop3_b32 v84, v69, s91, v68 bitop3:0xe4
	v_bfe_i32 v69, v150, 8, 1
	v_bitop3_b32 v68, v85, s91, v147 bitop3:0xe4
	v_bfe_i32 v147, v151, 8, 1
	v_bitop3_b32 v85, v70, s91, v69 bitop3:0xe4
	v_bfe_i32 v70, v150, 9, 1
	v_bitop3_b32 v69, v86, s91, v147 bitop3:0xe4
	v_bfe_i32 v86, v151, 9, 1
	v_bitop3_b32 v147, v71, s91, v70 bitop3:0xe4
	v_bfe_i32 v71, v150, 10, 1
	v_bitop3_b32 v70, v87, s91, v86 bitop3:0xe4
	v_bfe_i32 v86, v151, 10, 1
	v_bitop3_b32 v148, v72, s91, v71 bitop3:0xe4
	v_bfe_i32 v72, v150, 11, 1
	v_bitop3_b32 v71, v88, s91, v86 bitop3:0xe4
	v_bfe_i32 v86, v151, 11, 1
	v_bitop3_b32 v88, v73, s91, v72 bitop3:0xe4
	v_bfe_i32 v72, v150, 16, 1
	v_bitop3_b32 v73, v89, s91, v86 bitop3:0xe4
	v_bfe_i32 v86, v151, 16, 1
	v_bitop3_b32 v89, v74, s91, v72 bitop3:0xe4
	v_bfe_i32 v72, v150, 17, 1
	v_bfe_i32 v74, v151, 17, 1
	v_bitop3_b32 v86, v90, s91, v86 bitop3:0xe4
	v_bitop3_b32 v90, v75, s91, v72 bitop3:0xe4
	v_bitop3_b32 v87, v91, s91, v74 bitop3:0xe4
	v_bfe_i32 v72, v150, 18, 1
	v_bfe_i32 v74, v151, 18, 1
	v_bitop3_b32 v91, v76, s91, v72 bitop3:0xe4
	v_bitop3_b32 v76, v92, s91, v74 bitop3:0xe4
	v_bfe_i32 v72, v150, 19, 1
	v_bfe_i32 v74, v151, 19, 1
	v_bitop3_b32 v92, v77, s91, v72 bitop3:0xe4
	v_bitop3_b32 v77, v93, s91, v74 bitop3:0xe4
	v_bfe_i32 v72, v150, 24, 1
	v_bfe_i32 v74, v151, 24, 1
	v_bitop3_b32 v93, v78, s91, v72 bitop3:0xe4
	v_bitop3_b32 v78, v94, s91, v74 bitop3:0xe4
	v_bfe_i32 v72, v150, 25, 1
	v_bfe_i32 v74, v151, 25, 1
	v_bitop3_b32 v79, v79, s91, v72 bitop3:0xe4
	v_bitop3_b32 v72, v95, s91, v74 bitop3:0xe4
	v_bfe_i32 v74, v150, 26, 1
	v_bfe_i32 v75, v151, 26, 1
	v_bitop3_b32 v80, v80, s91, v74 bitop3:0xe4
	v_bitop3_b32 v74, v96, s91, v75 bitop3:0xe4
	v_bfe_i32 v75, v150, 27, 1
	v_bfe_i32 v94, v151, 27, 1
	v_bitop3_b32 v81, v81, s91, v75 bitop3:0xe4
	v_bitop3_b32 v75, v97, s91, v94 bitop3:0xe4
	v_max_f32_e32 v94, v82, v82
	v_max_f32_e32 v95, v146, v146
	v_max_f32_e32 v94, v95, v94
	v_max3_f32 v94, v94, v83, v84
	v_max3_f32 v94, v94, v85, v147
	v_max3_f32 v94, v94, v148, v88
	v_max3_f32 v94, v94, v89, v90
	v_max3_f32 v94, v94, v91, v92
	v_max3_f32 v94, v94, v93, v79
	v_max3_f32 v94, v94, v80, v81
	v_mfma_f32_32x32x16_bf16 v[18:33], v[156:159], v[206:209], v[18:33]
	v_max3_f32 v94, v94, v0, v66
	v_max3_f32 v94, v94, v67, v68
	v_max3_f32 v94, v94, v69, v70
	v_max3_f32 v94, v94, v71, v73
	v_max3_f32 v94, v94, v86, v87
	v_max3_f32 v94, v94, v76, v77
	v_max3_f32 v94, v94, v78, v72
	v_max3_f32 v94, v94, v74, v75
	v_mfma_f32_32x32x16_bf16 v[18:33], v[192:195], v[210:213], v[18:33]
	v_mov_b32_e32 v95, v94
	s_nop 1
	v_permlane32_swap_b32_e32 v94, v95
	v_max_f32_e32 v95, v95, v95
	v_max_f32_e32 v94, v94, v94
	v_max_f32_e32 v94, v94, v95
	v_sub_f32_e32 v95, v94, v152
	v_mul_f32_e32 v95, 0x3db504f3, v95
	v_cmp_ge_f32_e32 vcc, s92, v95
	v_max_f32_e32 v95, v152, v152
	v_max_f32_e32 v94, v95, v94
	v_mfma_f32_32x32x16_bf16 v[18:33], v[198:201], v[214:217], v[18:33]
	v_sub_f32_e32 v95, v152, v94
	v_mul_f32_e32 v95, 0x3e0293ee, v95
	v_exp_f32_e32 v95, v95
	s_cmp_eq_u64 vcc, exec
	s_cselect_b64 s[2:3], -1, 0
	s_barrier
; #define SBAR() __builtin_amdgcn_sched_barrier(0)
; #define VMW() asm volatile("s_waitcnt vmcnt(0)" ::: "memory")
; #define SWRITE_HV(bf) do { *(LAS bf16x8*)(V_lds + (bf) * SHM_V + vst0) = S.st_v0; *(LAS bf16x8*)(V_lds + (bf) * SHM_V + vst0 + 8192) = S.st_v1; } while (0)
; #define SWRITE_H(bf) do { SWRITE_HV(bf); SWRITE_HK(bf); } while (0)
; #define MLOAD(t) do { mw = Mb[moff + (unsigned)(t)]; } while (0)
; #define MASKT(P0_, P1_, t) do { mask_bits(P0_, P1_, mw, hi); } while (0)
; #define VMW() asm volatile("s_waitcnt vmcnt(0)" ::: "memory")
; __device__ __forceinline__ void attn_block(const unsigned char* wsb, const BlockRef& cur, const BlockRef& nxt, int skv, LAS char* lds, Seam& S, int wave_) {
;     ...
;     f32x16 pA0, pA1, pB0, pB1; float mnA, mnB, alA, alB; bf16x8 pa0, pa1, pa2, pa3;
;     SWRITE_HV(0); SBAR();
;     MLOAD(0);
;     if (NT > 1) SLOAD_H(Kh, Vh, KBASE(1));
;     SBAR(); qkt<0>(pA0, pA1, K_lds, r32, hi, S.qr);
;     MASKT(pA0, pA1, 0); partialSM(pA0, pA1, m_reg, mnA, alA);
;     if (NT > 1) { VMW(); SWRITE_H(1); }
;     __syncthreads();
	s_waitcnt vmcnt(0)
	v_cndmask_b32_e64 v191, v95, 1.0, s[2:3]
	v_cmp_gt_f32_e32 vcc, 1.0, v191
	s_waitcnt vmcnt(3)
	ds_write_b128 v180, v[130:133]
	s_waitcnt vmcnt(2)
	ds_write_b128 v180, v[134:137] offset:8192
	s_waitcnt vmcnt(1)
	ds_write_b128 v186, v[138:141] offset:32768
	s_waitcnt vmcnt(0)
	ds_write_b128 v186, v[142:145] offset:40960
	s_cbranch_vccz .LBB0_1597
	s_and_saveexec_b64 s[4:5], s[0:1]
	ds_write_b32 v185, v191 offset:128
	s_or_b64 exec, exec, s[4:5]
	s_waitcnt lgkmcnt(0)
	ds_read_b128 v[154:157], v184 offset:224
	ds_read_b128 v[158:161], v184 offset:192
	ds_read_b128 v[192:195], v184 offset:160
	ds_read_b128 v[198:201], v184 offset:128
	s_waitcnt lgkmcnt(3)
	v_pk_mul_f32 v[16:17], v[16:17], v[156:157]
	s_waitcnt lgkmcnt(2)
	v_pk_mul_f32 v[12:13], v[12:13], v[160:161]
	s_waitcnt lgkmcnt(1)
	v_pk_mul_f32 v[8:9], v[8:9], v[194:195]
	s_waitcnt lgkmcnt(0)
	v_pk_mul_f32 v[4:5], v[4:5], v[200:201]
	v_pk_mul_f32 v[14:15], v[14:15], v[154:155]
	v_pk_mul_f32 v[10:11], v[10:11], v[158:159]
	v_pk_mul_f32 v[6:7], v[6:7], v[192:193]
	v_pk_mul_f32 v[2:3], v[2:3], v[198:199]
	v_pk_mul_f32 v[64:65], v[64:65], v[156:157]
	v_pk_mul_f32 v[60:61], v[60:61], v[160:161]
	v_pk_mul_f32 v[56:57], v[56:57], v[194:195]
	v_pk_mul_f32 v[52:53], v[52:53], v[200:201]
	v_pk_mul_f32 v[62:63], v[62:63], v[154:155]
	v_pk_mul_f32 v[58:59], v[58:59], v[158:159]
	v_pk_mul_f32 v[54:55], v[54:55], v[192:193]
	v_pk_mul_f32 v[50:51], v[50:51], v[198:199]
	v_pk_mul_f32 v[48:49], v[48:49], v[156:157]
	v_pk_mul_f32 v[44:45], v[44:45], v[160:161]
	v_pk_mul_f32 v[40:41], v[40:41], v[194:195]
	v_pk_mul_f32 v[36:37], v[36:37], v[200:201]
	v_pk_mul_f32 v[46:47], v[46:47], v[154:155]
	v_pk_mul_f32 v[42:43], v[42:43], v[158:159]
	v_pk_mul_f32 v[38:39], v[38:39], v[192:193]
	v_pk_mul_f32 v[34:35], v[34:35], v[198:199]
	v_pk_mul_f32 v[32:33], v[32:33], v[156:157]
	v_pk_mul_f32 v[28:29], v[28:29], v[160:161]
	v_pk_mul_f32 v[24:25], v[24:25], v[194:195]
	v_pk_mul_f32 v[20:21], v[20:21], v[200:201]
	v_pk_mul_f32 v[30:31], v[30:31], v[154:155]
	v_pk_mul_f32 v[26:27], v[26:27], v[158:159]
	v_pk_mul_f32 v[22:23], v[22:23], v[192:193]
	v_pk_mul_f32 v[18:19], v[18:19], v[198:199]

; template <int VB>
; __device__ __forceinline__ void pv_tile(f32x16* o, int vb0, bf16x8 pa0, bf16x8 pa1, bf16x8 pa2, bf16x8 pa3) {
;     ...
;     PV_D0(0); PV_D0(1); PV_D0(2); PV_D0(3);
; __device__ __forceinline__ void attn_block(const unsigned char* wsb, const BlockRef& cur, const BlockRef& nxt, int skv, LAS char* lds, Seam& S, int wave_) {
;     ...
;     for (int t = 1; t + 1 < NT; t += 2) {
;         HALF_STEP(pB0, pB1, mnB, alB, pA0, pA1, alA, t, 1, 0, 0);
;         HALF_STEP(pA0, pA1, mnA, alA, pB0, pB1, alB, t + 1, 0, 1, 1);
.LBB0_1599:
	ds_read_b64_tr_b16 v[170:171], v178 offset:0x4000
	ds_read_b64_tr_b16 v[172:173], v178 offset:0x4800
	ds_read_b64_tr_b16 v[198:199], v178 offset:0x5000
	ds_read_b64_tr_b16 v[200:201], v178 offset:0x5800
	ds_read_b64_tr_b16 v[202:203], v178 offset:0x6000
	ds_read_b64_tr_b16 v[204:205], v178 offset:0x6800
	ds_read_b64_tr_b16 v[206:207], v178 offset:0x7000
	ds_read_b64_tr_b16 v[208:209], v178 offset:0x7800
	s_nop 0
	s_nop 0
	s_waitcnt lgkmcnt(6)
	v_mfma_f32_32x32x16_bf16 v[2:17], v[146:149], v[170:173], v[2:17]
	ds_read_b64_tr_b16 v[170:171], v178 offset:0x4200
	ds_read_b64_tr_b16 v[172:173], v178 offset:0x4a00
	s_waitcnt lgkmcnt(6)
	v_mfma_f32_32x32x16_bf16 v[2:17], v[150:153], v[198:201], v[2:17]
	ds_read_b64_tr_b16 v[198:199], v178 offset:0x5200
	ds_read_b64_tr_b16 v[200:201], v178 offset:0x5a00
	s_waitcnt lgkmcnt(6)
	v_mfma_f32_32x32x16_bf16 v[2:17], v[154:157], v[202:205], v[2:17]
	ds_read_b64_tr_b16 v[202:203], v178 offset:0x6200
	ds_read_b64_tr_b16 v[204:205], v178 offset:0x6a00
	s_waitcnt lgkmcnt(6)
	v_mfma_f32_32x32x16_bf16 v[2:17], v[158:161], v[206:209], v[2:17]
	ds_read_b64_tr_b16 v[206:207], v178 offset:0x7200
	ds_read_b64_tr_b16 v[208:209], v178 offset:0x7a00
	s_nop 0
	s_waitcnt lgkmcnt(6)
	v_mfma_f32_32x32x16_bf16 v[50:65], v[146:149], v[170:173], v[50:65]
	ds_read_b64_tr_b16 v[170:171], v178 offset:0x4400
	ds_read_b64_tr_b16 v[172:173], v178 offset:0x4c00
	s_waitcnt lgkmcnt(6)
	v_mfma_f32_32x32x16_bf16 v[50:65], v[150:153], v[198:201], v[50:65]
	ds_read_b64_tr_b16 v[198:199], v178 offset:0x5400
	ds_read_b64_tr_b16 v[200:201], v178 offset:0x5c00
	s_waitcnt lgkmcnt(6)
	v_mfma_f32_32x32x16_bf16 v[50:65], v[154:157], v[202:205], v[50:65]
	ds_read_b64_tr_b16 v[202:203], v178 offset:0x6400
	ds_read_b64_tr_b16 v[204:205], v178 offset:0x6c00
	s_waitcnt lgkmcnt(6)
	v_mfma_f32_32x32x16_bf16 v[50:65], v[158:161], v[206:209], v[50:65]
	ds_read_b64_tr_b16 v[206:207], v178 offset:0x7400
	ds_read_b64_tr_b16 v[208:209], v178 offset:0x7c00
	s_nop 0
	s_waitcnt lgkmcnt(6)
	v_mfma_f32_32x32x16_bf16 v[34:49], v[146:149], v[170:173], v[34:49]
	ds_read_b64_tr_b16 v[170:171], v178 offset:0x4600
	ds_read_b64_tr_b16 v[172:173], v178 offset:0x4e00
	s_waitcnt lgkmcnt(6)
	v_mfma_f32_32x32x16_bf16 v[34:49], v[150:153], v[198:201], v[34:49]
	ds_read_b64_tr_b16 v[198:199], v178 offset:0x5600
	ds_read_b64_tr_b16 v[200:201], v178 offset:0x5e00
	s_waitcnt lgkmcnt(6)
	v_mfma_f32_32x32x16_bf16 v[34:49], v[154:157], v[202:205], v[34:49]
	ds_read_b64_tr_b16 v[202:203], v178 offset:0x6600
	ds_read_b64_tr_b16 v[204:205], v178 offset:0x6e00
	s_waitcnt lgkmcnt(6)
	v_mfma_f32_32x32x16_bf16 v[34:49], v[158:161], v[206:209], v[34:49]
	ds_read_b64_tr_b16 v[206:207], v178 offset:0x7600
	ds_read_b64_tr_b16 v[208:209], v178 offset:0x7e00
	s_nop 0
	s_waitcnt lgkmcnt(6)
	v_mfma_f32_32x32x16_bf16 v[18:33], v[146:149], v[170:173], v[18:33]
	s_barrier
	v_mfma_f32_32x32x16_bf16 v[18:33], v[150:153], v[198:201], v[18:33]
	s_waitcnt vmcnt(4)
	v_lshrrev_b64 v[150:151], v166, v[174:175]
	v_bfe_i32 v146, v150, 0, 1
	v_bitop3_b32 v146, v82, s91, v146 bitop3:0xe4
	v_bfe_i32 v82, v150, 1, 1
	v_bitop3_b32 v147, v83, s91, v82 bitop3:0xe4
	v_bfe_i32 v82, v150, 2, 1
	v_bitop3_b32 v84, v84, s91, v82 bitop3:0xe4
	v_bfe_i32 v82, v150, 3, 1
	v_bitop3_b32 v85, v85, s91, v82 bitop3:0xe4
	v_bfe_i32 v82, v150, 8, 1
	v_bitop3_b32 v86, v86, s91, v82 bitop3:0xe4
	v_bfe_i32 v82, v150, 9, 1
	v_bitop3_b32 v87, v87, s91, v82 bitop3:0xe4
	v_bfe_i32 v82, v150, 10, 1
	v_bitop3_b32 v88, v88, s91, v82 bitop3:0xe4
	v_bfe_i32 v82, v150, 11, 1
	v_bitop3_b32 v89, v89, s91, v82 bitop3:0xe4
	v_bfe_i32 v82, v150, 16, 1
	v_bitop3_b32 v90, v90, s91, v82 bitop3:0xe4
	v_bfe_i32 v82, v150, 17, 1
	v_bitop3_b32 v91, v91, s91, v82 bitop3:0xe4
	v_bfe_i32 v82, v150, 18, 1
	v_bitop3_b32 v92, v92, s91, v82 bitop3:0xe4
	v_bfe_i32 v82, v150, 19, 1
	v_bitop3_b32 v93, v93, s91, v82 bitop3:0xe4
	v_bfe_i32 v82, v150, 24, 1
	v_bitop3_b32 v94, v94, s91, v82 bitop3:0xe4
	v_bfe_i32 v82, v150, 25, 1
	v_bitop3_b32 v95, v95, s91, v82 bitop3:0xe4
	v_bfe_i32 v82, v150, 26, 1
	v_bitop3_b32 v148, v96, s91, v82 bitop3:0xe4
	v_bfe_i32 v82, v150, 27, 1
	v_bfe_i32 v149, v151, 0, 1
	v_bfe_i32 v152, v151, 1, 1
	v_bitop3_b32 v96, v97, s91, v82 bitop3:0xe4
	v_max_f32_e32 v82, v147, v147
	v_max_f32_e32 v83, v146, v146
	v_max_f32_e32 v82, v83, v82
	v_bitop3_b32 v67, v67, s91, v152 bitop3:0xe4
	v_bitop3_b32 v66, v66, s91, v149 bitop3:0xe4
	v_max3_f32 v82, v82, v84, v85
	v_bfe_i32 v83, v151, 3, 1
	v_bfe_i32 v97, v151, 2, 1
	v_max3_f32 v82, v82, v86, v87
	v_max3_f32 v82, v82, v88, v89
	v_bitop3_b32 v69, v69, s91, v83 bitop3:0xe4
	v_bitop3_b32 v68, v68, s91, v97 bitop3:0xe4
	v_max3_f32 v82, v82, v90, v91
	v_bfe_i32 v83, v151, 9, 1
	v_bfe_i32 v97, v151, 8, 1
	v_max3_f32 v82, v82, v92, v93
	v_max3_f32 v82, v82, v94, v95
	v_bitop3_b32 v71, v71, s91, v83 bitop3:0xe4
	v_bitop3_b32 v70, v70, s91, v97 bitop3:0xe4
	v_max3_f32 v82, v82, v148, v96
	v_bfe_i32 v83, v151, 11, 1
	v_bfe_i32 v97, v151, 10, 1
	v_max3_f32 v82, v82, v66, v67
	v_max3_f32 v82, v82, v68, v69
	v_bitop3_b32 v73, v73, s91, v83 bitop3:0xe4
	v_bitop3_b32 v72, v72, s91, v97 bitop3:0xe4
	v_max3_f32 v82, v82, v70, v71
	v_max3_f32 v97, v82, v72, v73
	v_bfe_i32 v82, v151, 17, 1
	v_bfe_i32 v83, v151, 16, 1
	v_bitop3_b32 v75, v75, s91, v82 bitop3:0xe4
	v_bitop3_b32 v74, v74, s91, v83 bitop3:0xe4
	v_mov_b32_e32 v83, v75
	v_mov_b32_e32 v82, v74
	v_bfe_i32 v74, v151, 19, 1
	v_bfe_i32 v75, v151, 18, 1
	v_bitop3_b32 v74, v77, s91, v74 bitop3:0xe4
	v_bitop3_b32 v76, v76, s91, v75 bitop3:0xe4
	v_mov_b32_e32 v75, v74
	v_mov_b32_e32 v74, v76
	v_bfe_i32 v76, v151, 25, 1
	v_bfe_i32 v77, v151, 24, 1
	v_mfma_f32_32x32x16_bf16 v[18:33], v[154:157], v[202:205], v[18:33]
	v_bitop3_b32 v76, v79, s91, v76 bitop3:0xe4
	v_bitop3_b32 v78, v78, s91, v77 bitop3:0xe4
	v_mov_b32_e32 v77, v76
	v_mov_b32_e32 v76, v78
	v_bfe_i32 v78, v151, 27, 1
	v_bfe_i32 v79, v151, 26, 1
	v_max3_f32 v97, v97, v82, v83
	v_max3_f32 v97, v97, v74, v75
	v_bitop3_b32 v78, v81, s91, v78 bitop3:0xe4
	v_bitop3_b32 v80, v80, s91, v79 bitop3:0xe4
	v_max3_f32 v97, v97, v76, v77
	v_mov_b32_e32 v79, v78
	v_mov_b32_e32 v78, v80
	v_max3_f32 v80, v97, v78, v79
	v_mov_b32_e32 v81, v80
	v_mfma_f32_32x32x16_bf16 v[18:33], v[158:161], v[206:209], v[18:33]
	s_nop 0
	v_permlane32_swap_b32_e32 v80, v81
	v_max_f32_e32 v81, v81, v81
	v_max_f32_e32 v80, v80, v80
	v_max_f32_e32 v80, v80, v81
	v_sub_f32_e32 v81, v80, v192
	v_mul_f32_e32 v81, 0x3db504f3, v81
	v_cmp_ge_f32_e32 vcc, s92, v81
	s_cmp_eq_u64 vcc, exec
	s_cselect_b64 s[2:3], -1, 0
	s_andn2_b64 vcc, exec, s[4:5]
	s_cbranch_vccnz .LBB0_1601
	s_waitcnt vmcnt(0)
	ds_write_b128 v180, v[130:133] offset:16384
	ds_write_b128 v180, v[134:137] offset:24576
	ds_write_b128 v186, v[138:141] offset:49152
	ds_write_b128 v186, v[142:145] offset:57344
